# transposed snake chain order: the B fragment pair is held across four chains and the A pair is shared at the turns
# speedup vs baseline: 1.0006x; 1.0006x over previous
.LBB0_130:
	ds_read_b128 v[144:147], v140
	ds_read_b128 v[148:151], v140 offset:1024
	ds_read_b128 v[152:155], v140 offset:2048
	ds_read_b128 v[156:159], v140 offset:3072
	ds_read_b128 v[164:167], v141
	ds_read_b128 v[168:171], v141 offset:1024
	ds_read_b128 v[172:175], v141 offset:2048
	ds_read_b128 v[176:179], v141 offset:3072
	s_add_u32 s31, s10, 0xfff7c080
	s_addc_u32 s53, s11, -1
	s_cmp_eq_u32 s30, 28
	s_cselect_b32 s55, s25, s53
	s_cselect_b32 s54, s24, s31
	s_cselect_b32 s57, s4, s29
	s_cselect_b32 s56, s5, s28
	s_mov_b32 m0, s23
	ds_read_b128 v[180:183], v163
	ds_read_b128 v[190:193], v163 offset:1024
	ds_read_b128 v[194:197], v163 offset:2048
	ds_read_b128 v[198:201], v163 offset:3072
	ds_read_b128 v[202:205], v163 offset:4096
	ds_read_b128 v[206:209], v163 offset:5120
	ds_read_b128 v[216:219], v163 offset:6144
	ds_read_b128 v[220:223], v163 offset:7168
	global_load_lds_dwordx4 v138, s[10:11]
	s_mov_b32 m0, s33
	s_nop 0
	s_add_u32 s70, s10, s96
	s_addc_u32 s71, s11, s97
	global_load_lds_dwordx4 v138, s[70:71]
	s_waitcnt vmcnt(8)
	s_waitcnt lgkmcnt(0)
	s_barrier
	v_mfma_f32_16x16x32_bf16 v[120:123], v[144:147], v[180:183], v[120:123]
	v_mfma_f32_16x16x32_bf16 v[120:123], v[148:151], v[190:193], v[120:123]
	v_mfma_f32_16x16x32_bf16 v[104:107], v[144:147], v[194:197], v[104:107]
	v_mfma_f32_16x16x32_bf16 v[104:107], v[148:151], v[198:201], v[104:107]
	v_mfma_f32_16x16x32_bf16 v[88:91], v[144:147], v[202:205], v[88:91]
	v_mfma_f32_16x16x32_bf16 v[88:91], v[148:151], v[206:209], v[88:91]
	v_mfma_f32_16x16x32_bf16 v[72:75], v[144:147], v[216:219], v[72:75]
	v_mfma_f32_16x16x32_bf16 v[72:75], v[148:151], v[220:223], v[72:75]
	v_mfma_f32_16x16x32_bf16 v[68:71], v[152:155], v[216:219], v[68:71]
	v_mfma_f32_16x16x32_bf16 v[68:71], v[156:159], v[220:223], v[68:71]
	v_mfma_f32_16x16x32_bf16 v[84:87], v[152:155], v[202:205], v[84:87]
	v_mfma_f32_16x16x32_bf16 v[84:87], v[156:159], v[206:209], v[84:87]
	v_mfma_f32_16x16x32_bf16 v[100:103], v[152:155], v[194:197], v[100:103]
	v_mfma_f32_16x16x32_bf16 v[100:103], v[156:159], v[198:201], v[100:103]
	v_mfma_f32_16x16x32_bf16 v[116:119], v[152:155], v[180:183], v[116:119]
	v_mfma_f32_16x16x32_bf16 v[116:119], v[156:159], v[190:193], v[116:119]
	v_mfma_f32_16x16x32_bf16 v[124:127], v[172:175], v[180:183], v[124:127]
	v_mfma_f32_16x16x32_bf16 v[124:127], v[176:179], v[190:193], v[124:127]
	v_mfma_f32_16x16x32_bf16 v[108:111], v[172:175], v[194:197], v[108:111]
	v_mfma_f32_16x16x32_bf16 v[108:111], v[176:179], v[198:201], v[108:111]
	v_mfma_f32_16x16x32_bf16 v[92:95], v[172:175], v[202:205], v[92:95]
	v_mfma_f32_16x16x32_bf16 v[92:95], v[176:179], v[206:209], v[92:95]
	v_mfma_f32_16x16x32_bf16 v[76:79], v[172:175], v[216:219], v[76:79]
	v_mfma_f32_16x16x32_bf16 v[76:79], v[176:179], v[220:223], v[76:79]
	v_mfma_f32_16x16x32_bf16 v[80:83], v[164:167], v[216:219], v[80:83]
	v_mfma_f32_16x16x32_bf16 v[80:83], v[168:171], v[220:223], v[80:83]
	v_mfma_f32_16x16x32_bf16 v[96:99], v[164:167], v[202:205], v[96:99]
	v_mfma_f32_16x16x32_bf16 v[96:99], v[168:171], v[206:209], v[96:99]
	v_mfma_f32_16x16x32_bf16 v[112:115], v[164:167], v[194:197], v[112:115]
	v_mfma_f32_16x16x32_bf16 v[112:115], v[168:171], v[198:201], v[112:115]
	v_mfma_f32_16x16x32_bf16 v[128:131], v[164:167], v[180:183], v[128:131]
	v_mfma_f32_16x16x32_bf16 v[128:131], v[168:171], v[190:193], v[128:131]
	s_barrier
	s_mov_b32 m0, s45
	ds_read_b128 v[180:183], v163 offset:16384
	ds_read_b128 v[190:193], v163 offset:17408
	ds_read_b128 v[194:197], v163 offset:18432
	ds_read_b128 v[198:201], v163 offset:19456
	ds_read_b128 v[202:205], v163 offset:20480
	ds_read_b128 v[206:209], v163 offset:21504
	ds_read_b128 v[216:219], v163 offset:22528
	ds_read_b128 v[220:223], v163 offset:23552
	global_load_lds_dwordx4 v132, s[56:57]
	s_mov_b32 m0, s46
	s_nop 0
	s_add_u32 s70, s56, s90
	s_addc_u32 s71, s57, s91
	global_load_lds_dwordx4 v132, s[70:71]
	s_mov_b32 m0, s47
	s_nop 0
	s_add_u32 s70, s56, s60
	s_addc_u32 s71, s57, s61
	global_load_lds_dwordx4 v132, s[70:71]
	s_mov_b32 m0, s48
	s_nop 0
	s_add_u32 s70, s56, s64
	s_addc_u32 s71, s57, s65
	global_load_lds_dwordx4 v132, s[70:71]
	s_mov_b32 m0, s37
	s_nop 0
	global_load_lds_dwordx4 v134, s[54:55]
	s_mov_b32 m0, s38
	s_nop 0
	s_add_u32 s70, s54, s96
	s_addc_u32 s71, s55, s97
	global_load_lds_dwordx4 v134, s[70:71]
	s_waitcnt vmcnt(8)
	s_waitcnt lgkmcnt(0)
	s_barrier
	v_mfma_f32_16x16x32_bf16 v[56:59], v[144:147], v[180:183], v[56:59]
	v_mfma_f32_16x16x32_bf16 v[56:59], v[148:151], v[190:193], v[56:59]
	v_mfma_f32_16x16x32_bf16 v[40:43], v[144:147], v[194:197], v[40:43]
	v_mfma_f32_16x16x32_bf16 v[40:43], v[148:151], v[198:201], v[40:43]
	v_mfma_f32_16x16x32_bf16 v[24:27], v[144:147], v[202:205], v[24:27]
	v_mfma_f32_16x16x32_bf16 v[24:27], v[148:151], v[206:209], v[24:27]
	v_mfma_f32_16x16x32_bf16 v[8:11], v[144:147], v[216:219], v[8:11]
	v_mfma_f32_16x16x32_bf16 v[8:11], v[148:151], v[220:223], v[8:11]
	v_mfma_f32_16x16x32_bf16 v[4:7], v[152:155], v[216:219], v[4:7]
	v_mfma_f32_16x16x32_bf16 v[4:7], v[156:159], v[220:223], v[4:7]
	v_mfma_f32_16x16x32_bf16 v[20:23], v[152:155], v[202:205], v[20:23]
	v_mfma_f32_16x16x32_bf16 v[20:23], v[156:159], v[206:209], v[20:23]
	v_mfma_f32_16x16x32_bf16 v[36:39], v[152:155], v[194:197], v[36:39]
	v_mfma_f32_16x16x32_bf16 v[36:39], v[156:159], v[198:201], v[36:39]
	v_mfma_f32_16x16x32_bf16 v[52:55], v[152:155], v[180:183], v[52:55]
	v_mfma_f32_16x16x32_bf16 v[52:55], v[156:159], v[190:193], v[52:55]
	v_mfma_f32_16x16x32_bf16 v[60:63], v[172:175], v[180:183], v[60:63]
	v_mfma_f32_16x16x32_bf16 v[60:63], v[176:179], v[190:193], v[60:63]
	v_mfma_f32_16x16x32_bf16 v[44:47], v[172:175], v[194:197], v[44:47]
	v_mfma_f32_16x16x32_bf16 v[44:47], v[176:179], v[198:201], v[44:47]
	v_mfma_f32_16x16x32_bf16 v[28:31], v[172:175], v[202:205], v[28:31]
	v_mfma_f32_16x16x32_bf16 v[28:31], v[176:179], v[206:209], v[28:31]
	v_mfma_f32_16x16x32_bf16 v[12:15], v[172:175], v[216:219], v[12:15]
	v_mfma_f32_16x16x32_bf16 v[12:15], v[176:179], v[220:223], v[12:15]
	v_mfma_f32_16x16x32_bf16 v[16:19], v[164:167], v[216:219], v[16:19]
	v_mfma_f32_16x16x32_bf16 v[16:19], v[168:171], v[220:223], v[16:19]
	v_mfma_f32_16x16x32_bf16 v[32:35], v[164:167], v[202:205], v[32:35]
	v_mfma_f32_16x16x32_bf16 v[32:35], v[168:171], v[206:209], v[32:35]
	v_mfma_f32_16x16x32_bf16 v[48:51], v[164:167], v[194:197], v[48:51]
	v_mfma_f32_16x16x32_bf16 v[48:51], v[168:171], v[198:201], v[48:51]
	v_mfma_f32_16x16x32_bf16 v[64:67], v[164:167], v[180:183], v[64:67]
	v_mfma_f32_16x16x32_bf16 v[64:67], v[168:171], v[190:193], v[64:67]
	s_barrier
; #define PG8_MMA(ai, bj, At, Bt) do { __builtin_amdgcn_s_setprio(1); _Pragma("unroll") for (int m = 0; m < 4; ++m) _Pragma("unroll") for (int n = 0; n < 2; ++n) _Pragma("unroll") for (int k = 0; k < 2; ++k) \
;         acc[ai][bj][m][n] = __builtin_amdgcn_mfma_f32_16x16x32_bf16(Bt[n][k], At[m][k], acc[ai][bj][m][n], 0, 0, 0); __builtin_amdgcn_s_setprio(0); } while (0)
; #define PG8_WAIT_V(n) asm volatile("s_waitcnt vmcnt(" #n ")" ::: "memory")
; #define PG8_TRIP_HEAD(T) const int t = (T); const bool last = (t == nt - 2); \
;             const char* a1 = cA + (size_t)(t + 1) * kstep; \
;             const char* a2 = last ? nA : cA + (size_t)(t + 2) * kstep; const char* b2 = last ? nB : cB + (size_t)(t + 2) * kstep; \
;             const char* a3 = a2 + kstep; const char* b3 = b2 + kstep; \
;             if (last && has_next) S.a_ready(nxt);
; template <class Epi, class Sched, bool ALIGN_EPI = false, bool SP2 = false>
; __device__ __forceinline__ void gemm_phase(PG8_LAS unsigned char* lds, const Gemm g, const Sched& S, const Epi& E) {
;     ...
;         if constexpr (SP2) {
;             { PG8_TRIP_HEAD(0) PG8_TRIP_SP2(asm volatile("s_waitcnt vmcnt(%0)" :: "n"(8 + Epi::NST) : "memory"), PG8_MMAZ) }
;             for (int tt = 2; tt < nt; tt += 2) { PG8_TRIP_HEAD(tt) PG8_TRIP_SP2(PG8_WAIT_V(8), PG8_MMA) }
	ds_read_b128 v[144:147], v142
	ds_read_b128 v[148:151], v142 offset:1024
	ds_read_b128 v[152:155], v142 offset:2048
	ds_read_b128 v[156:159], v142 offset:3072
	ds_read_b128 v[164:167], v143
	ds_read_b128 v[168:171], v143 offset:1024
	ds_read_b128 v[172:175], v143 offset:2048
	ds_read_b128 v[176:179], v143 offset:3072
	s_mov_b32 m0, s39
	ds_read_b128 v[180:183], v163 offset:32768
	ds_read_b128 v[190:193], v163 offset:33792
	ds_read_b128 v[194:197], v163 offset:34816
	ds_read_b128 v[198:201], v163 offset:35840
	ds_read_b128 v[202:205], v163 offset:36864
	ds_read_b128 v[206:209], v163 offset:37888
	ds_read_b128 v[216:219], v163 offset:38912
	ds_read_b128 v[220:223], v163 offset:39936
	s_add_u32 s70, s54, s82
	s_addc_u32 s71, s55, s83
	global_load_lds_dwordx4 v134, s[70:71]
	s_mov_b32 m0, s40
	s_nop 0
	s_add_u32 s70, s54, s68
	s_addc_u32 s71, s55, s69
	global_load_lds_dwordx4 v134, s[70:71]
	s_waitcnt vmcnt(8)
	s_waitcnt lgkmcnt(0)
	s_barrier
	v_mfma_f32_16x16x32_bf16 v[120:123], v[144:147], v[180:183], v[120:123]
	v_mfma_f32_16x16x32_bf16 v[120:123], v[148:151], v[190:193], v[120:123]
	v_mfma_f32_16x16x32_bf16 v[104:107], v[144:147], v[194:197], v[104:107]
	v_mfma_f32_16x16x32_bf16 v[104:107], v[148:151], v[198:201], v[104:107]
	v_mfma_f32_16x16x32_bf16 v[88:91], v[144:147], v[202:205], v[88:91]
	v_mfma_f32_16x16x32_bf16 v[88:91], v[148:151], v[206:209], v[88:91]
	v_mfma_f32_16x16x32_bf16 v[72:75], v[144:147], v[216:219], v[72:75]
	v_mfma_f32_16x16x32_bf16 v[72:75], v[148:151], v[220:223], v[72:75]
	v_mfma_f32_16x16x32_bf16 v[68:71], v[152:155], v[216:219], v[68:71]
	v_mfma_f32_16x16x32_bf16 v[68:71], v[156:159], v[220:223], v[68:71]
	v_mfma_f32_16x16x32_bf16 v[84:87], v[152:155], v[202:205], v[84:87]
	v_mfma_f32_16x16x32_bf16 v[84:87], v[156:159], v[206:209], v[84:87]
	v_mfma_f32_16x16x32_bf16 v[100:103], v[152:155], v[194:197], v[100:103]
	v_mfma_f32_16x16x32_bf16 v[100:103], v[156:159], v[198:201], v[100:103]
	v_mfma_f32_16x16x32_bf16 v[116:119], v[152:155], v[180:183], v[116:119]
	v_mfma_f32_16x16x32_bf16 v[116:119], v[156:159], v[190:193], v[116:119]
	v_mfma_f32_16x16x32_bf16 v[124:127], v[172:175], v[180:183], v[124:127]
	v_mfma_f32_16x16x32_bf16 v[124:127], v[176:179], v[190:193], v[124:127]
	v_mfma_f32_16x16x32_bf16 v[108:111], v[172:175], v[194:197], v[108:111]
	v_mfma_f32_16x16x32_bf16 v[108:111], v[176:179], v[198:201], v[108:111]
	v_mfma_f32_16x16x32_bf16 v[92:95], v[172:175], v[202:205], v[92:95]
	v_mfma_f32_16x16x32_bf16 v[92:95], v[176:179], v[206:209], v[92:95]
	v_mfma_f32_16x16x32_bf16 v[76:79], v[172:175], v[216:219], v[76:79]
	v_mfma_f32_16x16x32_bf16 v[76:79], v[176:179], v[220:223], v[76:79]
	v_mfma_f32_16x16x32_bf16 v[80:83], v[164:167], v[216:219], v[80:83]
	v_mfma_f32_16x16x32_bf16 v[80:83], v[168:171], v[220:223], v[80:83]
	v_mfma_f32_16x16x32_bf16 v[96:99], v[164:167], v[202:205], v[96:99]
	v_mfma_f32_16x16x32_bf16 v[96:99], v[168:171], v[206:209], v[96:99]
	v_mfma_f32_16x16x32_bf16 v[112:115], v[164:167], v[194:197], v[112:115]
	v_mfma_f32_16x16x32_bf16 v[112:115], v[168:171], v[198:201], v[112:115]
	v_mfma_f32_16x16x32_bf16 v[128:131], v[164:167], v[180:183], v[128:131]
	v_mfma_f32_16x16x32_bf16 v[128:131], v[168:171], v[190:193], v[128:131]
	s_barrier
	s_mov_b32 m0, s49
	ds_read_b128 v[180:183], v163 offset:49152
	ds_read_b128 v[190:193], v163 offset:50176
	ds_read_b128 v[194:197], v163 offset:51200
	ds_read_b128 v[198:201], v163 offset:52224
	ds_read_b128 v[202:205], v163 offset:53248
	ds_read_b128 v[206:209], v163 offset:54272
	ds_read_b128 v[216:219], v163 offset:55296
	ds_read_b128 v[220:223], v163 offset:56320
	s_add_u32 s70, s56, s78
	s_addc_u32 s71, s57, s79
	global_load_lds_dwordx4 v132, s[70:71]
	s_mov_b32 m0, s50
	s_nop 0
	s_add_u32 s70, s56, s84
	s_addc_u32 s71, s57, s85
	global_load_lds_dwordx4 v132, s[70:71]
	s_mov_b32 m0, s51
	s_add_u32 s70, s56, s62
	s_addc_u32 s71, s57, s63
	global_load_lds_dwordx4 v132, s[70:71]
	s_mov_b32 m0, s52
	s_nop 0
	s_add_u32 s70, s56, s66
	s_addc_u32 s71, s57, s67
	global_load_lds_dwordx4 v132, s[70:71]
	s_mov_b32 m0, s0
	s_nop 0
	s_add_u32 s70, s54, s78
	s_addc_u32 s71, s55, s79
	global_load_lds_dwordx4 v134, s[70:71]
	s_mov_b32 m0, s41
	s_nop 0
	s_add_u32 s70, s54, s92
	s_addc_u32 s71, s55, s93
	global_load_lds_dwordx4 v134, s[70:71]
	s_waitcnt vmcnt(8)
	s_waitcnt lgkmcnt(0)
	s_barrier
	v_mfma_f32_16x16x32_bf16 v[56:59], v[144:147], v[180:183], v[56:59]
	v_mfma_f32_16x16x32_bf16 v[56:59], v[148:151], v[190:193], v[56:59]
	v_mfma_f32_16x16x32_bf16 v[40:43], v[144:147], v[194:197], v[40:43]
	v_mfma_f32_16x16x32_bf16 v[40:43], v[148:151], v[198:201], v[40:43]
	v_mfma_f32_16x16x32_bf16 v[24:27], v[144:147], v[202:205], v[24:27]
	v_mfma_f32_16x16x32_bf16 v[24:27], v[148:151], v[206:209], v[24:27]
	v_mfma_f32_16x16x32_bf16 v[8:11], v[144:147], v[216:219], v[8:11]
	v_mfma_f32_16x16x32_bf16 v[8:11], v[148:151], v[220:223], v[8:11]
	v_mfma_f32_16x16x32_bf16 v[4:7], v[152:155], v[216:219], v[4:7]
	v_mfma_f32_16x16x32_bf16 v[4:7], v[156:159], v[220:223], v[4:7]
	v_mfma_f32_16x16x32_bf16 v[20:23], v[152:155], v[202:205], v[20:23]
	v_mfma_f32_16x16x32_bf16 v[20:23], v[156:159], v[206:209], v[20:23]
	v_mfma_f32_16x16x32_bf16 v[36:39], v[152:155], v[194:197], v[36:39]
	v_mfma_f32_16x16x32_bf16 v[36:39], v[156:159], v[198:201], v[36:39]
	v_mfma_f32_16x16x32_bf16 v[52:55], v[152:155], v[180:183], v[52:55]
	v_mfma_f32_16x16x32_bf16 v[52:55], v[156:159], v[190:193], v[52:55]
	v_mfma_f32_16x16x32_bf16 v[60:63], v[172:175], v[180:183], v[60:63]
	v_mfma_f32_16x16x32_bf16 v[60:63], v[176:179], v[190:193], v[60:63]
	v_mfma_f32_16x16x32_bf16 v[44:47], v[172:175], v[194:197], v[44:47]
	v_mfma_f32_16x16x32_bf16 v[44:47], v[176:179], v[198:201], v[44:47]
	v_mfma_f32_16x16x32_bf16 v[28:31], v[172:175], v[202:205], v[28:31]
	v_mfma_f32_16x16x32_bf16 v[28:31], v[176:179], v[206:209], v[28:31]
	v_mfma_f32_16x16x32_bf16 v[12:15], v[172:175], v[216:219], v[12:15]
	v_mfma_f32_16x16x32_bf16 v[12:15], v[176:179], v[220:223], v[12:15]
	v_mfma_f32_16x16x32_bf16 v[16:19], v[164:167], v[216:219], v[16:19]
	v_mfma_f32_16x16x32_bf16 v[16:19], v[168:171], v[220:223], v[16:19]
	v_mfma_f32_16x16x32_bf16 v[32:35], v[164:167], v[202:205], v[32:35]
	v_mfma_f32_16x16x32_bf16 v[32:35], v[168:171], v[206:209], v[32:35]
	v_mfma_f32_16x16x32_bf16 v[48:51], v[164:167], v[194:197], v[48:51]
	v_mfma_f32_16x16x32_bf16 v[48:51], v[168:171], v[198:201], v[48:51]
	v_mfma_f32_16x16x32_bf16 v[64:67], v[164:167], v[180:183], v[64:67]
	v_mfma_f32_16x16x32_bf16 v[64:67], v[168:171], v[190:193], v[64:67]
	s_barrier
	s_add_i32 s30, s30, 2
	s_add_u32 s10, s10, 0x100
	s_addc_u32 s11, s11, 0
	s_add_u32 s28, s28, 0x100
	s_addc_u32 s29, s29, 0
	s_cmp_gt_u32 s30, 29
	s_cbranch_scc0 .LBB0_130
	s_and_b64 vcc, exec, s[20:21]
	s_cbranch_vccz .LBB0_133
	s_barrier

.LBB0_233:
	ds_read_b128 v[120:123], v116
	ds_read_b128 v[132:135], v116 offset:1024
	ds_read_b128 v[144:147], v116 offset:2048
	ds_read_b128 v[148:151], v116 offset:3072
	ds_read_b128 v[152:155], v117
	ds_read_b128 v[156:159], v117 offset:1024
	ds_read_b128 v[166:169], v117 offset:2048
	ds_read_b128 v[170:173], v117 offset:3072
	s_add_u32 s49, s26, 0xffea0080
	s_addc_u32 s50, s27, -1
	s_cmpk_eq_i32 s48, 0x54
	s_cselect_b32 s51, s21, s50
	s_cselect_b32 s50, s20, s49
	s_cselect_b32 s53, s23, s25
	s_cselect_b32 s52, s22, s24
	s_mov_b32 m0, s0
	ds_read_b128 v[180:183], v178
	ds_read_b128 v[184:187], v178 offset:1024
	ds_read_b128 v[190:193], v178 offset:2048
	ds_read_b128 v[194:197], v178 offset:3072
	ds_read_b128 v[198:201], v178 offset:4096
	ds_read_b128 v[202:205], v178 offset:5120
	ds_read_b128 v[206:209], v178 offset:6144
	ds_read_b128 v[216:219], v178 offset:7168
	global_load_lds_dwordx4 v164, s[26:27]
	s_mov_b32 m0, s4
	s_nop 0
	s_add_u32 s70, s26, s86
	s_addc_u32 s71, s27, s87
	global_load_lds_dwordx4 v164, s[70:71]
	s_waitcnt vmcnt(8)
	s_waitcnt lgkmcnt(0)
	s_barrier
	v_mfma_f32_16x16x32_bf16 v[140:143], v[120:123], v[180:183], v[140:143]
	v_mfma_f32_16x16x32_bf16 v[140:143], v[132:135], v[184:187], v[140:143]
	v_mfma_f32_16x16x32_bf16 v[112:115], v[120:123], v[190:193], v[112:115]
	v_mfma_f32_16x16x32_bf16 v[112:115], v[132:135], v[194:197], v[112:115]
	v_mfma_f32_16x16x32_bf16 v[96:99], v[120:123], v[198:201], v[96:99]
	v_mfma_f32_16x16x32_bf16 v[96:99], v[132:135], v[202:205], v[96:99]
	v_mfma_f32_16x16x32_bf16 v[80:83], v[120:123], v[206:209], v[80:83]
	v_mfma_f32_16x16x32_bf16 v[80:83], v[132:135], v[216:219], v[80:83]
	v_mfma_f32_16x16x32_bf16 v[76:79], v[144:147], v[206:209], v[76:79]
	v_mfma_f32_16x16x32_bf16 v[76:79], v[148:151], v[216:219], v[76:79]
	v_mfma_f32_16x16x32_bf16 v[92:95], v[144:147], v[198:201], v[92:95]
	v_mfma_f32_16x16x32_bf16 v[92:95], v[148:151], v[202:205], v[92:95]
	v_mfma_f32_16x16x32_bf16 v[108:111], v[144:147], v[190:193], v[108:111]
	v_mfma_f32_16x16x32_bf16 v[108:111], v[148:151], v[194:197], v[108:111]
	v_mfma_f32_16x16x32_bf16 v[136:139], v[144:147], v[180:183], v[136:139]
	v_mfma_f32_16x16x32_bf16 v[136:139], v[148:151], v[184:187], v[136:139]
	v_mfma_f32_16x16x32_bf16 v[124:127], v[166:169], v[180:183], v[124:127]
	v_mfma_f32_16x16x32_bf16 v[124:127], v[170:173], v[184:187], v[124:127]
	v_mfma_f32_16x16x32_bf16 v[100:103], v[166:169], v[190:193], v[100:103]
	v_mfma_f32_16x16x32_bf16 v[100:103], v[170:173], v[194:197], v[100:103]
	v_mfma_f32_16x16x32_bf16 v[84:87], v[166:169], v[198:201], v[84:87]
	v_mfma_f32_16x16x32_bf16 v[84:87], v[170:173], v[202:205], v[84:87]
	v_mfma_f32_16x16x32_bf16 v[68:71], v[166:169], v[206:209], v[68:71]
	v_mfma_f32_16x16x32_bf16 v[68:71], v[170:173], v[216:219], v[68:71]
	v_mfma_f32_16x16x32_bf16 v[72:75], v[152:155], v[206:209], v[72:75]
	v_mfma_f32_16x16x32_bf16 v[72:75], v[156:159], v[216:219], v[72:75]
	v_mfma_f32_16x16x32_bf16 v[88:91], v[152:155], v[198:201], v[88:91]
	v_mfma_f32_16x16x32_bf16 v[88:91], v[156:159], v[202:205], v[88:91]
	v_mfma_f32_16x16x32_bf16 v[104:107], v[152:155], v[190:193], v[104:107]
	v_mfma_f32_16x16x32_bf16 v[104:107], v[156:159], v[194:197], v[104:107]
	v_mfma_f32_16x16x32_bf16 v[128:131], v[152:155], v[180:183], v[128:131]
	v_mfma_f32_16x16x32_bf16 v[128:131], v[156:159], v[184:187], v[128:131]
	s_barrier
	s_mov_b32 m0, s5
	ds_read_b128 v[180:183], v178 offset:16384
	ds_read_b128 v[184:187], v178 offset:17408
	ds_read_b128 v[190:193], v178 offset:18432
	ds_read_b128 v[194:197], v178 offset:19456
	ds_read_b128 v[198:201], v178 offset:20480
	ds_read_b128 v[202:205], v178 offset:21504
	ds_read_b128 v[206:209], v178 offset:22528
	ds_read_b128 v[216:219], v178 offset:23552
	global_load_lds_dwordx4 v162, s[52:53]
	s_mov_b32 m0, s33
	s_nop 0
	s_add_u32 s70, s52, s86
	s_addc_u32 s71, s53, s87
	global_load_lds_dwordx4 v162, s[70:71]
	s_mov_b32 m0, s42
	s_nop 0
	s_add_u32 s70, s52, s54
	s_addc_u32 s71, s53, s55
	global_load_lds_dwordx4 v162, s[70:71]
	s_mov_b32 m0, s43
	s_nop 0
	s_add_u32 s70, s52, s56
	s_addc_u32 s71, s53, s57
	global_load_lds_dwordx4 v162, s[70:71]
	s_mov_b32 m0, s31
	s_nop 0
	global_load_lds_dwordx4 v160, s[50:51]
	s_mov_b32 m0, s34
	s_nop 0
	s_add_u32 s70, s50, s86
	s_addc_u32 s71, s51, s87
	global_load_lds_dwordx4 v160, s[70:71]
	s_waitcnt vmcnt(8)
	s_waitcnt lgkmcnt(0)
	s_barrier
	v_mfma_f32_16x16x32_bf16 v[56:59], v[120:123], v[180:183], v[56:59]
	v_mfma_f32_16x16x32_bf16 v[56:59], v[132:135], v[184:187], v[56:59]
	v_mfma_f32_16x16x32_bf16 v[48:51], v[120:123], v[190:193], v[48:51]
	v_mfma_f32_16x16x32_bf16 v[48:51], v[132:135], v[194:197], v[48:51]
	v_mfma_f32_16x16x32_bf16 v[32:35], v[120:123], v[198:201], v[32:35]
	v_mfma_f32_16x16x32_bf16 v[32:35], v[132:135], v[202:205], v[32:35]
	v_mfma_f32_16x16x32_bf16 v[16:19], v[120:123], v[206:209], v[16:19]
	v_mfma_f32_16x16x32_bf16 v[16:19], v[132:135], v[216:219], v[16:19]
	v_mfma_f32_16x16x32_bf16 v[12:15], v[144:147], v[206:209], v[12:15]
	v_mfma_f32_16x16x32_bf16 v[12:15], v[148:151], v[216:219], v[12:15]
	v_mfma_f32_16x16x32_bf16 v[28:31], v[144:147], v[198:201], v[28:31]
	v_mfma_f32_16x16x32_bf16 v[28:31], v[148:151], v[202:205], v[28:31]
	v_mfma_f32_16x16x32_bf16 v[44:47], v[144:147], v[190:193], v[44:47]
	v_mfma_f32_16x16x32_bf16 v[44:47], v[148:151], v[194:197], v[44:47]
	v_mfma_f32_16x16x32_bf16 v[52:55], v[144:147], v[180:183], v[52:55]
	v_mfma_f32_16x16x32_bf16 v[52:55], v[148:151], v[184:187], v[52:55]
	v_mfma_f32_16x16x32_bf16 v[60:63], v[166:169], v[180:183], v[60:63]
	v_mfma_f32_16x16x32_bf16 v[60:63], v[170:173], v[184:187], v[60:63]
	v_mfma_f32_16x16x32_bf16 v[36:39], v[166:169], v[190:193], v[36:39]
	v_mfma_f32_16x16x32_bf16 v[36:39], v[170:173], v[194:197], v[36:39]
	v_mfma_f32_16x16x32_bf16 v[20:23], v[166:169], v[198:201], v[20:23]
	v_mfma_f32_16x16x32_bf16 v[20:23], v[170:173], v[202:205], v[20:23]
	v_mfma_f32_16x16x32_bf16 v[4:7], v[166:169], v[206:209], v[4:7]
	v_mfma_f32_16x16x32_bf16 v[4:7], v[170:173], v[216:219], v[4:7]
	v_mfma_f32_16x16x32_bf16 v[8:11], v[152:155], v[206:209], v[8:11]
	v_mfma_f32_16x16x32_bf16 v[8:11], v[156:159], v[216:219], v[8:11]
	v_mfma_f32_16x16x32_bf16 v[24:27], v[152:155], v[198:201], v[24:27]
	v_mfma_f32_16x16x32_bf16 v[24:27], v[156:159], v[202:205], v[24:27]
	v_mfma_f32_16x16x32_bf16 v[40:43], v[152:155], v[190:193], v[40:43]
	v_mfma_f32_16x16x32_bf16 v[40:43], v[156:159], v[194:197], v[40:43]
	v_mfma_f32_16x16x32_bf16 v[64:67], v[152:155], v[180:183], v[64:67]
	v_mfma_f32_16x16x32_bf16 v[64:67], v[156:159], v[184:187], v[64:67]
	s_barrier
; #define PG8_MMA(ai, bj, At, Bt) do { __builtin_amdgcn_s_setprio(1); _Pragma("unroll") for (int m = 0; m < 4; ++m) _Pragma("unroll") for (int n = 0; n < 2; ++n) _Pragma("unroll") for (int k = 0; k < 2; ++k) \
;         acc[ai][bj][m][n] = __builtin_amdgcn_mfma_f32_16x16x32_bf16(Bt[n][k], At[m][k], acc[ai][bj][m][n], 0, 0, 0); __builtin_amdgcn_s_setprio(0); } while (0)
; #define PG8_WAIT_V(n) asm volatile("s_waitcnt vmcnt(" #n ")" ::: "memory")
; #define PG8_TRIP_HEAD(T) const int t = (T); const bool last = (t == nt - 2); \
;             const char* a1 = cA + (size_t)(t + 1) * kstep; \
;             const char* a2 = last ? nA : cA + (size_t)(t + 2) * kstep; const char* b2 = last ? nB : cB + (size_t)(t + 2) * kstep; \
;             const char* a3 = a2 + kstep; const char* b3 = b2 + kstep; \
;             if (last && has_next) S.a_ready(nxt);
; template <class Epi, class Sched, bool ALIGN_EPI = false, bool SP2 = false>
; __device__ __forceinline__ void gemm_phase(PG8_LAS unsigned char* lds, const Gemm g, const Sched& S, const Epi& E) {
;     ...
;         if constexpr (SP2) {
;             { PG8_TRIP_HEAD(0) PG8_TRIP_SP2(asm volatile("s_waitcnt vmcnt(%0)" :: "n"(8 + Epi::NST) : "memory"), PG8_MMAZ) }
;             for (int tt = 2; tt < nt; tt += 2) { PG8_TRIP_HEAD(tt) PG8_TRIP_SP2(PG8_WAIT_V(8), PG8_MMA) }
	ds_read_b128 v[120:123], v118
	ds_read_b128 v[132:135], v118 offset:1024
	ds_read_b128 v[144:147], v118 offset:2048
	ds_read_b128 v[148:151], v118 offset:3072
	ds_read_b128 v[152:155], v119
	ds_read_b128 v[156:159], v119 offset:1024
	ds_read_b128 v[166:169], v119 offset:2048
	ds_read_b128 v[170:173], v119 offset:3072
	s_mov_b32 m0, s35
	ds_read_b128 v[180:183], v178 offset:32768
	ds_read_b128 v[184:187], v178 offset:33792
	ds_read_b128 v[190:193], v178 offset:34816
	ds_read_b128 v[194:197], v178 offset:35840
	ds_read_b128 v[198:201], v178 offset:36864
	ds_read_b128 v[202:205], v178 offset:37888
	ds_read_b128 v[206:209], v178 offset:38912
	ds_read_b128 v[216:219], v178 offset:39936
	s_add_u32 s70, s50, s54
	s_addc_u32 s71, s51, s55
	global_load_lds_dwordx4 v160, s[70:71]
	s_mov_b32 m0, s36
	s_nop 0
	s_add_u32 s70, s50, s56
	s_addc_u32 s71, s51, s57
	global_load_lds_dwordx4 v160, s[70:71]
	s_waitcnt vmcnt(8)
	s_waitcnt lgkmcnt(0)
	s_barrier
	v_mfma_f32_16x16x32_bf16 v[140:143], v[120:123], v[180:183], v[140:143]
	v_mfma_f32_16x16x32_bf16 v[140:143], v[132:135], v[184:187], v[140:143]
	v_mfma_f32_16x16x32_bf16 v[112:115], v[120:123], v[190:193], v[112:115]
	v_mfma_f32_16x16x32_bf16 v[112:115], v[132:135], v[194:197], v[112:115]
	v_mfma_f32_16x16x32_bf16 v[96:99], v[120:123], v[198:201], v[96:99]
	v_mfma_f32_16x16x32_bf16 v[96:99], v[132:135], v[202:205], v[96:99]
	v_mfma_f32_16x16x32_bf16 v[80:83], v[120:123], v[206:209], v[80:83]
	v_mfma_f32_16x16x32_bf16 v[80:83], v[132:135], v[216:219], v[80:83]
	v_mfma_f32_16x16x32_bf16 v[76:79], v[144:147], v[206:209], v[76:79]
	v_mfma_f32_16x16x32_bf16 v[76:79], v[148:151], v[216:219], v[76:79]
	v_mfma_f32_16x16x32_bf16 v[92:95], v[144:147], v[198:201], v[92:95]
	v_mfma_f32_16x16x32_bf16 v[92:95], v[148:151], v[202:205], v[92:95]
	v_mfma_f32_16x16x32_bf16 v[108:111], v[144:147], v[190:193], v[108:111]
	v_mfma_f32_16x16x32_bf16 v[108:111], v[148:151], v[194:197], v[108:111]
	v_mfma_f32_16x16x32_bf16 v[136:139], v[144:147], v[180:183], v[136:139]
	v_mfma_f32_16x16x32_bf16 v[136:139], v[148:151], v[184:187], v[136:139]
	v_mfma_f32_16x16x32_bf16 v[124:127], v[166:169], v[180:183], v[124:127]
	v_mfma_f32_16x16x32_bf16 v[124:127], v[170:173], v[184:187], v[124:127]
	v_mfma_f32_16x16x32_bf16 v[100:103], v[166:169], v[190:193], v[100:103]
	v_mfma_f32_16x16x32_bf16 v[100:103], v[170:173], v[194:197], v[100:103]
	v_mfma_f32_16x16x32_bf16 v[84:87], v[166:169], v[198:201], v[84:87]
	v_mfma_f32_16x16x32_bf16 v[84:87], v[170:173], v[202:205], v[84:87]
	v_mfma_f32_16x16x32_bf16 v[68:71], v[166:169], v[206:209], v[68:71]
	v_mfma_f32_16x16x32_bf16 v[68:71], v[170:173], v[216:219], v[68:71]
	v_mfma_f32_16x16x32_bf16 v[72:75], v[152:155], v[206:209], v[72:75]
	v_mfma_f32_16x16x32_bf16 v[72:75], v[156:159], v[216:219], v[72:75]
	v_mfma_f32_16x16x32_bf16 v[88:91], v[152:155], v[198:201], v[88:91]
	v_mfma_f32_16x16x32_bf16 v[88:91], v[156:159], v[202:205], v[88:91]
	v_mfma_f32_16x16x32_bf16 v[104:107], v[152:155], v[190:193], v[104:107]
	v_mfma_f32_16x16x32_bf16 v[104:107], v[156:159], v[194:197], v[104:107]
	v_mfma_f32_16x16x32_bf16 v[128:131], v[152:155], v[180:183], v[128:131]
	v_mfma_f32_16x16x32_bf16 v[128:131], v[156:159], v[184:187], v[128:131]
	s_barrier
	s_mov_b32 m0, s44
	ds_read_b128 v[180:183], v178 offset:49152
	ds_read_b128 v[184:187], v178 offset:50176
	ds_read_b128 v[190:193], v178 offset:51200
	ds_read_b128 v[194:197], v178 offset:52224
	ds_read_b128 v[198:201], v178 offset:53248
	ds_read_b128 v[202:205], v178 offset:54272
	ds_read_b128 v[206:209], v178 offset:55296
	ds_read_b128 v[216:219], v178 offset:56320
	s_add_u32 s70, s52, s78
	s_addc_u32 s71, s53, s79
	global_load_lds_dwordx4 v162, s[70:71]
	s_mov_b32 m0, s45
	s_nop 0
	s_add_u32 s70, s52, s60
	s_addc_u32 s71, s53, s61
	global_load_lds_dwordx4 v162, s[70:71]
	s_mov_b32 m0, s46
	s_add_u32 s70, s52, s62
	s_addc_u32 s71, s53, s63
	global_load_lds_dwordx4 v162, s[70:71]
	s_mov_b32 m0, s47
	s_nop 0
	s_add_u32 s70, s52, s64
	s_addc_u32 s71, s53, s65
	global_load_lds_dwordx4 v162, s[70:71]
	s_mov_b32 m0, s37
	s_nop 0
	s_add_u32 s70, s50, s78
	s_addc_u32 s71, s51, s79
	global_load_lds_dwordx4 v160, s[70:71]
	s_mov_b32 m0, s38
	s_nop 0
	s_add_u32 s70, s50, s60
	s_addc_u32 s71, s51, s61
	global_load_lds_dwordx4 v160, s[70:71]
	s_waitcnt vmcnt(8)
	s_waitcnt lgkmcnt(0)
	s_barrier
	v_mfma_f32_16x16x32_bf16 v[56:59], v[120:123], v[180:183], v[56:59]
	v_mfma_f32_16x16x32_bf16 v[56:59], v[132:135], v[184:187], v[56:59]
	v_mfma_f32_16x16x32_bf16 v[48:51], v[120:123], v[190:193], v[48:51]
	v_mfma_f32_16x16x32_bf16 v[48:51], v[132:135], v[194:197], v[48:51]
	v_mfma_f32_16x16x32_bf16 v[32:35], v[120:123], v[198:201], v[32:35]
	v_mfma_f32_16x16x32_bf16 v[32:35], v[132:135], v[202:205], v[32:35]
	v_mfma_f32_16x16x32_bf16 v[16:19], v[120:123], v[206:209], v[16:19]
	v_mfma_f32_16x16x32_bf16 v[16:19], v[132:135], v[216:219], v[16:19]
	v_mfma_f32_16x16x32_bf16 v[12:15], v[144:147], v[206:209], v[12:15]
	v_mfma_f32_16x16x32_bf16 v[12:15], v[148:151], v[216:219], v[12:15]
	v_mfma_f32_16x16x32_bf16 v[28:31], v[144:147], v[198:201], v[28:31]
	v_mfma_f32_16x16x32_bf16 v[28:31], v[148:151], v[202:205], v[28:31]
	v_mfma_f32_16x16x32_bf16 v[44:47], v[144:147], v[190:193], v[44:47]
	v_mfma_f32_16x16x32_bf16 v[44:47], v[148:151], v[194:197], v[44:47]
	v_mfma_f32_16x16x32_bf16 v[52:55], v[144:147], v[180:183], v[52:55]
	v_mfma_f32_16x16x32_bf16 v[52:55], v[148:151], v[184:187], v[52:55]
	v_mfma_f32_16x16x32_bf16 v[60:63], v[166:169], v[180:183], v[60:63]
	v_mfma_f32_16x16x32_bf16 v[60:63], v[170:173], v[184:187], v[60:63]
	v_mfma_f32_16x16x32_bf16 v[36:39], v[166:169], v[190:193], v[36:39]
	v_mfma_f32_16x16x32_bf16 v[36:39], v[170:173], v[194:197], v[36:39]
	v_mfma_f32_16x16x32_bf16 v[20:23], v[166:169], v[198:201], v[20:23]
	v_mfma_f32_16x16x32_bf16 v[20:23], v[170:173], v[202:205], v[20:23]
	v_mfma_f32_16x16x32_bf16 v[4:7], v[166:169], v[206:209], v[4:7]
	v_mfma_f32_16x16x32_bf16 v[4:7], v[170:173], v[216:219], v[4:7]
	v_mfma_f32_16x16x32_bf16 v[8:11], v[152:155], v[206:209], v[8:11]
	v_mfma_f32_16x16x32_bf16 v[8:11], v[156:159], v[216:219], v[8:11]
	v_mfma_f32_16x16x32_bf16 v[24:27], v[152:155], v[198:201], v[24:27]
	v_mfma_f32_16x16x32_bf16 v[24:27], v[156:159], v[202:205], v[24:27]
	v_mfma_f32_16x16x32_bf16 v[40:43], v[152:155], v[190:193], v[40:43]
	v_mfma_f32_16x16x32_bf16 v[40:43], v[156:159], v[194:197], v[40:43]
	v_mfma_f32_16x16x32_bf16 v[64:67], v[152:155], v[180:183], v[64:67]
	v_mfma_f32_16x16x32_bf16 v[64:67], v[156:159], v[184:187], v[64:67]
	s_barrier
	s_add_i32 s48, s48, 2
	s_add_u32 s26, s26, 0x100
	s_addc_u32 s27, s27, 0
	s_add_u32 s24, s24, 0x100
	s_addc_u32 s25, s25, 0
	s_cmpk_gt_u32 s48, 0x55
	s_cbranch_scc0 .LBB0_233
	s_and_b64 vcc, exec, s[18:19]
	s_cbranch_vccz .LBB0_236
	s_barrier

.LBB0_324:
	ds_read_b128 v[136:139], v132
	ds_read_b128 v[140:143], v132 offset:1024
	ds_read_b128 v[144:147], v132 offset:2048
	ds_read_b128 v[148:151], v132 offset:3072
	ds_read_b128 v[152:155], v133
	ds_read_b128 v[156:159], v133 offset:1024
	ds_read_b128 v[160:163], v133 offset:2048
	ds_read_b128 v[174:177], v133 offset:3072
	s_add_u32 s15, s10, 0xfff7c080
	s_addc_u32 s50, s11, -1
	s_cmp_eq_u32 s14, 28
	s_cselect_b32 s51, s25, s50
	s_cselect_b32 s50, s24, s15
	s_cselect_b32 s53, s3, s13
	s_cselect_b32 s52, s4, s12
	s_mov_b32 m0, s5
	ds_read_b128 v[178:181], v200
	ds_read_b128 v[182:185], v200 offset:1024
	ds_read_b128 v[186:189], v200 offset:2048
	ds_read_b128 v[190:193], v200 offset:3072
	ds_read_b128 v[202:205], v200 offset:4096
	ds_read_b128 v[206:209], v200 offset:5120
	ds_read_b128 v[216:219], v200 offset:6144
	ds_read_b128 v[220:223], v200 offset:7168
	global_load_lds_dwordx4 v172, s[10:11]
	s_mov_b32 m0, s23
	s_nop 0
	s_add_u32 s70, s10, s96
	s_addc_u32 s71, s11, s97
	global_load_lds_dwordx4 v172, s[70:71]
	s_waitcnt vmcnt(8)
	s_waitcnt lgkmcnt(0)
	s_barrier
	v_mfma_f32_16x16x32_bf16 v[120:123], v[136:139], v[178:181], v[120:123]
	v_mfma_f32_16x16x32_bf16 v[120:123], v[140:143], v[182:185], v[120:123]
	v_mfma_f32_16x16x32_bf16 v[104:107], v[136:139], v[186:189], v[104:107]
	v_mfma_f32_16x16x32_bf16 v[104:107], v[140:143], v[190:193], v[104:107]
	v_mfma_f32_16x16x32_bf16 v[88:91], v[136:139], v[202:205], v[88:91]
	v_mfma_f32_16x16x32_bf16 v[88:91], v[140:143], v[206:209], v[88:91]
	v_mfma_f32_16x16x32_bf16 v[72:75], v[136:139], v[216:219], v[72:75]
	v_mfma_f32_16x16x32_bf16 v[72:75], v[140:143], v[220:223], v[72:75]
	v_mfma_f32_16x16x32_bf16 v[68:71], v[144:147], v[216:219], v[68:71]
	v_mfma_f32_16x16x32_bf16 v[68:71], v[148:151], v[220:223], v[68:71]
	v_mfma_f32_16x16x32_bf16 v[84:87], v[144:147], v[202:205], v[84:87]
	v_mfma_f32_16x16x32_bf16 v[84:87], v[148:151], v[206:209], v[84:87]
	v_mfma_f32_16x16x32_bf16 v[100:103], v[144:147], v[186:189], v[100:103]
	v_mfma_f32_16x16x32_bf16 v[100:103], v[148:151], v[190:193], v[100:103]
	v_mfma_f32_16x16x32_bf16 v[116:119], v[144:147], v[178:181], v[116:119]
	v_mfma_f32_16x16x32_bf16 v[116:119], v[148:151], v[182:185], v[116:119]
	v_mfma_f32_16x16x32_bf16 v[124:127], v[160:163], v[178:181], v[124:127]
	v_mfma_f32_16x16x32_bf16 v[124:127], v[174:177], v[182:185], v[124:127]
	v_mfma_f32_16x16x32_bf16 v[108:111], v[160:163], v[186:189], v[108:111]
	v_mfma_f32_16x16x32_bf16 v[108:111], v[174:177], v[190:193], v[108:111]
	v_mfma_f32_16x16x32_bf16 v[92:95], v[160:163], v[202:205], v[92:95]
	v_mfma_f32_16x16x32_bf16 v[92:95], v[174:177], v[206:209], v[92:95]
	v_mfma_f32_16x16x32_bf16 v[76:79], v[160:163], v[216:219], v[76:79]
	v_mfma_f32_16x16x32_bf16 v[76:79], v[174:177], v[220:223], v[76:79]
	v_mfma_f32_16x16x32_bf16 v[80:83], v[152:155], v[216:219], v[80:83]
	v_mfma_f32_16x16x32_bf16 v[80:83], v[156:159], v[220:223], v[80:83]
	v_mfma_f32_16x16x32_bf16 v[96:99], v[152:155], v[202:205], v[96:99]
	v_mfma_f32_16x16x32_bf16 v[96:99], v[156:159], v[206:209], v[96:99]
	v_mfma_f32_16x16x32_bf16 v[112:115], v[152:155], v[186:189], v[112:115]
	v_mfma_f32_16x16x32_bf16 v[112:115], v[156:159], v[190:193], v[112:115]
	v_mfma_f32_16x16x32_bf16 v[128:131], v[152:155], v[178:181], v[128:131]
	v_mfma_f32_16x16x32_bf16 v[128:131], v[156:159], v[182:185], v[128:131]
	s_barrier
	s_mov_b32 m0, s28
	ds_read_b128 v[178:181], v200 offset:16384
	ds_read_b128 v[182:185], v200 offset:17408
	ds_read_b128 v[186:189], v200 offset:18432
	ds_read_b128 v[190:193], v200 offset:19456
	ds_read_b128 v[202:205], v200 offset:20480
	ds_read_b128 v[206:209], v200 offset:21504
	ds_read_b128 v[216:219], v200 offset:22528
	ds_read_b128 v[220:223], v200 offset:23552
	global_load_lds_dwordx4 v164, s[52:53]
	s_mov_b32 m0, s29
	s_nop 0
	s_add_u32 s70, s52, s90
	s_addc_u32 s71, s53, s91
	global_load_lds_dwordx4 v164, s[70:71]
	s_mov_b32 m0, s33
	s_nop 0
	s_add_u32 s70, s52, s54
	s_addc_u32 s71, s53, s55
	global_load_lds_dwordx4 v164, s[70:71]
	s_mov_b32 m0, s45
	s_nop 0
	s_add_u32 s70, s52, s60
	s_addc_u32 s71, s53, s61
	global_load_lds_dwordx4 v164, s[70:71]
	s_mov_b32 m0, s30
	s_nop 0
	global_load_lds_dwordx4 v166, s[50:51]
	s_mov_b32 m0, s31
	s_nop 0
	s_add_u32 s70, s50, s96
	s_addc_u32 s71, s51, s97
	global_load_lds_dwordx4 v166, s[70:71]
	s_waitcnt vmcnt(8)
	s_waitcnt lgkmcnt(0)
	s_barrier
	v_mfma_f32_16x16x32_bf16 v[56:59], v[136:139], v[178:181], v[56:59]
	v_mfma_f32_16x16x32_bf16 v[56:59], v[140:143], v[182:185], v[56:59]
	v_mfma_f32_16x16x32_bf16 v[40:43], v[136:139], v[186:189], v[40:43]
	v_mfma_f32_16x16x32_bf16 v[40:43], v[140:143], v[190:193], v[40:43]
	v_mfma_f32_16x16x32_bf16 v[24:27], v[136:139], v[202:205], v[24:27]
	v_mfma_f32_16x16x32_bf16 v[24:27], v[140:143], v[206:209], v[24:27]
	v_mfma_f32_16x16x32_bf16 v[8:11], v[136:139], v[216:219], v[8:11]
	v_mfma_f32_16x16x32_bf16 v[8:11], v[140:143], v[220:223], v[8:11]
	v_mfma_f32_16x16x32_bf16 v[4:7], v[144:147], v[216:219], v[4:7]
	v_mfma_f32_16x16x32_bf16 v[4:7], v[148:151], v[220:223], v[4:7]
	v_mfma_f32_16x16x32_bf16 v[20:23], v[144:147], v[202:205], v[20:23]
	v_mfma_f32_16x16x32_bf16 v[20:23], v[148:151], v[206:209], v[20:23]
	v_mfma_f32_16x16x32_bf16 v[36:39], v[144:147], v[186:189], v[36:39]
	v_mfma_f32_16x16x32_bf16 v[36:39], v[148:151], v[190:193], v[36:39]
	v_mfma_f32_16x16x32_bf16 v[52:55], v[144:147], v[178:181], v[52:55]
	v_mfma_f32_16x16x32_bf16 v[52:55], v[148:151], v[182:185], v[52:55]
	v_mfma_f32_16x16x32_bf16 v[60:63], v[160:163], v[178:181], v[60:63]
	v_mfma_f32_16x16x32_bf16 v[60:63], v[174:177], v[182:185], v[60:63]
	v_mfma_f32_16x16x32_bf16 v[44:47], v[160:163], v[186:189], v[44:47]
	v_mfma_f32_16x16x32_bf16 v[44:47], v[174:177], v[190:193], v[44:47]
	v_mfma_f32_16x16x32_bf16 v[28:31], v[160:163], v[202:205], v[28:31]
	v_mfma_f32_16x16x32_bf16 v[28:31], v[174:177], v[206:209], v[28:31]
	v_mfma_f32_16x16x32_bf16 v[12:15], v[160:163], v[216:219], v[12:15]
	v_mfma_f32_16x16x32_bf16 v[12:15], v[174:177], v[220:223], v[12:15]
	v_mfma_f32_16x16x32_bf16 v[16:19], v[152:155], v[216:219], v[16:19]
	v_mfma_f32_16x16x32_bf16 v[16:19], v[156:159], v[220:223], v[16:19]
	v_mfma_f32_16x16x32_bf16 v[32:35], v[152:155], v[202:205], v[32:35]
	v_mfma_f32_16x16x32_bf16 v[32:35], v[156:159], v[206:209], v[32:35]
	v_mfma_f32_16x16x32_bf16 v[48:51], v[152:155], v[186:189], v[48:51]
	v_mfma_f32_16x16x32_bf16 v[48:51], v[156:159], v[190:193], v[48:51]
	v_mfma_f32_16x16x32_bf16 v[64:67], v[152:155], v[178:181], v[64:67]
	v_mfma_f32_16x16x32_bf16 v[64:67], v[156:159], v[182:185], v[64:67]
	s_barrier
; #define PG8_MMA(ai, bj, At, Bt) do { __builtin_amdgcn_s_setprio(1); _Pragma("unroll") for (int m = 0; m < 4; ++m) _Pragma("unroll") for (int n = 0; n < 2; ++n) _Pragma("unroll") for (int k = 0; k < 2; ++k) \
;         acc[ai][bj][m][n] = __builtin_amdgcn_mfma_f32_16x16x32_bf16(Bt[n][k], At[m][k], acc[ai][bj][m][n], 0, 0, 0); __builtin_amdgcn_s_setprio(0); } while (0)
; #define PG8_WAIT_V(n) asm volatile("s_waitcnt vmcnt(" #n ")" ::: "memory")
; #define PG8_TRIP_HEAD(T) const int t = (T); const bool last = (t == nt - 2); \
;             const char* a1 = cA + (size_t)(t + 1) * kstep; \
;             const char* a2 = last ? nA : cA + (size_t)(t + 2) * kstep; const char* b2 = last ? nB : cB + (size_t)(t + 2) * kstep; \
;             const char* a3 = a2 + kstep; const char* b3 = b2 + kstep; \
;             if (last && has_next) S.a_ready(nxt);
; template <class Epi, class Sched, bool ALIGN_EPI = false, bool SP2 = false>
; __device__ __forceinline__ void gemm_phase(PG8_LAS unsigned char* lds, const Gemm g, const Sched& S, const Epi& E) {
;     ...
;         if constexpr (SP2) {
;             { PG8_TRIP_HEAD(0) PG8_TRIP_SP2(asm volatile("s_waitcnt vmcnt(%0)" :: "n"(8 + Epi::NST) : "memory"), PG8_MMAZ) }
;             for (int tt = 2; tt < nt; tt += 2) { PG8_TRIP_HEAD(tt) PG8_TRIP_SP2(PG8_WAIT_V(8), PG8_MMA) }
	ds_read_b128 v[136:139], v134
	ds_read_b128 v[140:143], v134 offset:1024
	ds_read_b128 v[144:147], v134 offset:2048
	ds_read_b128 v[148:151], v134 offset:3072
	ds_read_b128 v[152:155], v135
	ds_read_b128 v[156:159], v135 offset:1024
	ds_read_b128 v[160:163], v135 offset:2048
	ds_read_b128 v[174:177], v135 offset:3072
	s_mov_b32 m0, s34
	ds_read_b128 v[178:181], v200 offset:32768
	ds_read_b128 v[182:185], v200 offset:33792
	ds_read_b128 v[186:189], v200 offset:34816
	ds_read_b128 v[190:193], v200 offset:35840
	ds_read_b128 v[202:205], v200 offset:36864
	ds_read_b128 v[206:209], v200 offset:37888
	ds_read_b128 v[216:219], v200 offset:38912
	ds_read_b128 v[220:223], v200 offset:39936
	s_add_u32 s70, s50, s82
	s_addc_u32 s71, s51, s83
	global_load_lds_dwordx4 v166, s[70:71]
	s_mov_b32 m0, s35
	s_nop 0
	s_add_u32 s70, s50, s64
	s_addc_u32 s71, s51, s65
	global_load_lds_dwordx4 v166, s[70:71]
	s_waitcnt vmcnt(8)
	s_waitcnt lgkmcnt(0)
	s_barrier
	v_mfma_f32_16x16x32_bf16 v[120:123], v[136:139], v[178:181], v[120:123]
	v_mfma_f32_16x16x32_bf16 v[120:123], v[140:143], v[182:185], v[120:123]
	v_mfma_f32_16x16x32_bf16 v[104:107], v[136:139], v[186:189], v[104:107]
	v_mfma_f32_16x16x32_bf16 v[104:107], v[140:143], v[190:193], v[104:107]
	v_mfma_f32_16x16x32_bf16 v[88:91], v[136:139], v[202:205], v[88:91]
	v_mfma_f32_16x16x32_bf16 v[88:91], v[140:143], v[206:209], v[88:91]
	v_mfma_f32_16x16x32_bf16 v[72:75], v[136:139], v[216:219], v[72:75]
	v_mfma_f32_16x16x32_bf16 v[72:75], v[140:143], v[220:223], v[72:75]
	v_mfma_f32_16x16x32_bf16 v[68:71], v[144:147], v[216:219], v[68:71]
	v_mfma_f32_16x16x32_bf16 v[68:71], v[148:151], v[220:223], v[68:71]
	v_mfma_f32_16x16x32_bf16 v[84:87], v[144:147], v[202:205], v[84:87]
	v_mfma_f32_16x16x32_bf16 v[84:87], v[148:151], v[206:209], v[84:87]
	v_mfma_f32_16x16x32_bf16 v[100:103], v[144:147], v[186:189], v[100:103]
	v_mfma_f32_16x16x32_bf16 v[100:103], v[148:151], v[190:193], v[100:103]
	v_mfma_f32_16x16x32_bf16 v[116:119], v[144:147], v[178:181], v[116:119]
	v_mfma_f32_16x16x32_bf16 v[116:119], v[148:151], v[182:185], v[116:119]
	v_mfma_f32_16x16x32_bf16 v[124:127], v[160:163], v[178:181], v[124:127]
	v_mfma_f32_16x16x32_bf16 v[124:127], v[174:177], v[182:185], v[124:127]
	v_mfma_f32_16x16x32_bf16 v[108:111], v[160:163], v[186:189], v[108:111]
	v_mfma_f32_16x16x32_bf16 v[108:111], v[174:177], v[190:193], v[108:111]
	v_mfma_f32_16x16x32_bf16 v[92:95], v[160:163], v[202:205], v[92:95]
	v_mfma_f32_16x16x32_bf16 v[92:95], v[174:177], v[206:209], v[92:95]
	v_mfma_f32_16x16x32_bf16 v[76:79], v[160:163], v[216:219], v[76:79]
	v_mfma_f32_16x16x32_bf16 v[76:79], v[174:177], v[220:223], v[76:79]
	v_mfma_f32_16x16x32_bf16 v[80:83], v[152:155], v[216:219], v[80:83]
	v_mfma_f32_16x16x32_bf16 v[80:83], v[156:159], v[220:223], v[80:83]
	v_mfma_f32_16x16x32_bf16 v[96:99], v[152:155], v[202:205], v[96:99]
	v_mfma_f32_16x16x32_bf16 v[96:99], v[156:159], v[206:209], v[96:99]
	v_mfma_f32_16x16x32_bf16 v[112:115], v[152:155], v[186:189], v[112:115]
	v_mfma_f32_16x16x32_bf16 v[112:115], v[156:159], v[190:193], v[112:115]
	v_mfma_f32_16x16x32_bf16 v[128:131], v[152:155], v[178:181], v[128:131]
	v_mfma_f32_16x16x32_bf16 v[128:131], v[156:159], v[182:185], v[128:131]
	s_barrier
	s_mov_b32 m0, s46
	ds_read_b128 v[178:181], v200 offset:49152
	ds_read_b128 v[182:185], v200 offset:50176
	ds_read_b128 v[186:189], v200 offset:51200
	ds_read_b128 v[190:193], v200 offset:52224
	ds_read_b128 v[202:205], v200 offset:53248
	ds_read_b128 v[206:209], v200 offset:54272
	ds_read_b128 v[216:219], v200 offset:55296
	ds_read_b128 v[220:223], v200 offset:56320
	s_add_u32 s70, s52, s78
	s_addc_u32 s71, s53, s79
	global_load_lds_dwordx4 v164, s[70:71]
	s_mov_b32 m0, s47
	s_nop 0
	s_add_u32 s70, s52, s84
	s_addc_u32 s71, s53, s85
	global_load_lds_dwordx4 v164, s[70:71]
	s_mov_b32 m0, s48
	s_add_u32 s70, s52, s56
	s_addc_u32 s71, s53, s57
	global_load_lds_dwordx4 v164, s[70:71]
	s_mov_b32 m0, s49
	s_nop 0
	s_add_u32 s70, s52, s62
	s_addc_u32 s71, s53, s63
	global_load_lds_dwordx4 v164, s[70:71]
	s_mov_b32 m0, s38
	s_nop 0
	s_add_u32 s70, s50, s78
	s_addc_u32 s71, s51, s79
	global_load_lds_dwordx4 v166, s[70:71]
	s_mov_b32 m0, s39
	s_nop 0
	s_add_u32 s70, s50, s92
	s_addc_u32 s71, s51, s93
	global_load_lds_dwordx4 v166, s[70:71]
	s_waitcnt vmcnt(8)
	s_waitcnt lgkmcnt(0)
	s_barrier
	v_mfma_f32_16x16x32_bf16 v[56:59], v[136:139], v[178:181], v[56:59]
	v_mfma_f32_16x16x32_bf16 v[56:59], v[140:143], v[182:185], v[56:59]
	v_mfma_f32_16x16x32_bf16 v[40:43], v[136:139], v[186:189], v[40:43]
	v_mfma_f32_16x16x32_bf16 v[40:43], v[140:143], v[190:193], v[40:43]
	v_mfma_f32_16x16x32_bf16 v[24:27], v[136:139], v[202:205], v[24:27]
	v_mfma_f32_16x16x32_bf16 v[24:27], v[140:143], v[206:209], v[24:27]
	v_mfma_f32_16x16x32_bf16 v[8:11], v[136:139], v[216:219], v[8:11]
	v_mfma_f32_16x16x32_bf16 v[8:11], v[140:143], v[220:223], v[8:11]
	v_mfma_f32_16x16x32_bf16 v[4:7], v[144:147], v[216:219], v[4:7]
	v_mfma_f32_16x16x32_bf16 v[4:7], v[148:151], v[220:223], v[4:7]
	v_mfma_f32_16x16x32_bf16 v[20:23], v[144:147], v[202:205], v[20:23]
	v_mfma_f32_16x16x32_bf16 v[20:23], v[148:151], v[206:209], v[20:23]
	v_mfma_f32_16x16x32_bf16 v[36:39], v[144:147], v[186:189], v[36:39]
	v_mfma_f32_16x16x32_bf16 v[36:39], v[148:151], v[190:193], v[36:39]
	v_mfma_f32_16x16x32_bf16 v[52:55], v[144:147], v[178:181], v[52:55]
	v_mfma_f32_16x16x32_bf16 v[52:55], v[148:151], v[182:185], v[52:55]
	v_mfma_f32_16x16x32_bf16 v[60:63], v[160:163], v[178:181], v[60:63]
	v_mfma_f32_16x16x32_bf16 v[60:63], v[174:177], v[182:185], v[60:63]
	v_mfma_f32_16x16x32_bf16 v[44:47], v[160:163], v[186:189], v[44:47]
	v_mfma_f32_16x16x32_bf16 v[44:47], v[174:177], v[190:193], v[44:47]
	v_mfma_f32_16x16x32_bf16 v[28:31], v[160:163], v[202:205], v[28:31]
	v_mfma_f32_16x16x32_bf16 v[28:31], v[174:177], v[206:209], v[28:31]
	v_mfma_f32_16x16x32_bf16 v[12:15], v[160:163], v[216:219], v[12:15]
	v_mfma_f32_16x16x32_bf16 v[12:15], v[174:177], v[220:223], v[12:15]
	v_mfma_f32_16x16x32_bf16 v[16:19], v[152:155], v[216:219], v[16:19]
	v_mfma_f32_16x16x32_bf16 v[16:19], v[156:159], v[220:223], v[16:19]
	v_mfma_f32_16x16x32_bf16 v[32:35], v[152:155], v[202:205], v[32:35]
	v_mfma_f32_16x16x32_bf16 v[32:35], v[156:159], v[206:209], v[32:35]
	v_mfma_f32_16x16x32_bf16 v[48:51], v[152:155], v[186:189], v[48:51]
	v_mfma_f32_16x16x32_bf16 v[48:51], v[156:159], v[190:193], v[48:51]
	v_mfma_f32_16x16x32_bf16 v[64:67], v[152:155], v[178:181], v[64:67]
	v_mfma_f32_16x16x32_bf16 v[64:67], v[156:159], v[182:185], v[64:67]
	s_barrier
	s_add_i32 s14, s14, 2
	s_add_u32 s10, s10, 0x100
	s_addc_u32 s11, s11, 0
	s_add_u32 s12, s12, 0x100
	s_addc_u32 s13, s13, 0
	s_cmp_gt_u32 s14, 29
	s_cbranch_scc0 .LBB0_324
	s_and_b64 vcc, exec, s[18:19]
	s_cbranch_vccz .LBB0_327
	s_barrier

.LBB0_594:
	ds_read_b128 v[136:139], v116
	ds_read_b128 v[140:143], v116 offset:1024
	ds_read_b128 v[144:147], v116 offset:2048
	ds_read_b128 v[148:151], v116 offset:3072
	ds_read_b128 v[152:155], v117
	ds_read_b128 v[156:159], v117 offset:1024
	ds_read_b128 v[160:163], v117 offset:2048
	ds_read_b128 v[164:167], v117 offset:3072
	s_add_u32 s43, s20, 0xfff7c080
	s_addc_u32 s44, s21, -1
	s_cmp_eq_u32 s15, 28
	s_cselect_b32 s45, s17, s44
	s_cselect_b32 s44, s16, s43
	s_cselect_b32 s47, s4, s9
	s_cselect_b32 s46, s5, s8
	s_mov_b32 m0, s33
	ds_read_b128 v[168:171], v221
	ds_read_b128 v[172:175], v221 offset:1024
	ds_read_b128 v[176:179], v221 offset:2048
	ds_read_b128 v[180:183], v221 offset:3072
	ds_read_b128 v[184:187], v221 offset:4096
	ds_read_b128 v[188:191], v221 offset:5120
	ds_read_b128 v[202:205], v221 offset:6144
	ds_read_b128 v[206:209], v221 offset:7168
	global_load_lds_dwordx4 v200, s[20:21]
	s_mov_b32 m0, s34
	s_nop 0
	s_add_u32 s70, s20, s96
	s_addc_u32 s71, s21, s97
	global_load_lds_dwordx4 v200, s[70:71]
	s_waitcnt vmcnt(8)
	s_waitcnt lgkmcnt(0)
	s_barrier
	v_mfma_f32_16x16x32_bf16 v[130:133], v[136:139], v[168:171], v[130:133]
	v_mfma_f32_16x16x32_bf16 v[130:133], v[140:143], v[172:175], v[130:133]
	v_mfma_f32_16x16x32_bf16 v[112:115], v[136:139], v[176:179], v[112:115]
	v_mfma_f32_16x16x32_bf16 v[112:115], v[140:143], v[180:183], v[112:115]
	v_mfma_f32_16x16x32_bf16 v[96:99], v[136:139], v[184:187], v[96:99]
	v_mfma_f32_16x16x32_bf16 v[96:99], v[140:143], v[188:191], v[96:99]
	v_mfma_f32_16x16x32_bf16 v[80:83], v[136:139], v[202:205], v[80:83]
	v_mfma_f32_16x16x32_bf16 v[80:83], v[140:143], v[206:209], v[80:83]
	v_mfma_f32_16x16x32_bf16 v[76:79], v[144:147], v[202:205], v[76:79]
	v_mfma_f32_16x16x32_bf16 v[76:79], v[148:151], v[206:209], v[76:79]
	v_mfma_f32_16x16x32_bf16 v[92:95], v[144:147], v[184:187], v[92:95]
	v_mfma_f32_16x16x32_bf16 v[92:95], v[148:151], v[188:191], v[92:95]
	v_mfma_f32_16x16x32_bf16 v[108:111], v[144:147], v[176:179], v[108:111]
	v_mfma_f32_16x16x32_bf16 v[108:111], v[148:151], v[180:183], v[108:111]
	v_mfma_f32_16x16x32_bf16 v[126:129], v[144:147], v[168:171], v[126:129]
	v_mfma_f32_16x16x32_bf16 v[126:129], v[148:151], v[172:175], v[126:129]
	v_mfma_f32_16x16x32_bf16 v[118:121], v[160:163], v[168:171], v[118:121]
	v_mfma_f32_16x16x32_bf16 v[118:121], v[164:167], v[172:175], v[118:121]
	v_mfma_f32_16x16x32_bf16 v[100:103], v[160:163], v[176:179], v[100:103]
	v_mfma_f32_16x16x32_bf16 v[100:103], v[164:167], v[180:183], v[100:103]
	v_mfma_f32_16x16x32_bf16 v[84:87], v[160:163], v[184:187], v[84:87]
	v_mfma_f32_16x16x32_bf16 v[84:87], v[164:167], v[188:191], v[84:87]
	v_mfma_f32_16x16x32_bf16 v[68:71], v[160:163], v[202:205], v[68:71]
	v_mfma_f32_16x16x32_bf16 v[68:71], v[164:167], v[206:209], v[68:71]
	v_mfma_f32_16x16x32_bf16 v[72:75], v[152:155], v[202:205], v[72:75]
	v_mfma_f32_16x16x32_bf16 v[72:75], v[156:159], v[206:209], v[72:75]
	v_mfma_f32_16x16x32_bf16 v[88:91], v[152:155], v[184:187], v[88:91]
	v_mfma_f32_16x16x32_bf16 v[88:91], v[156:159], v[188:191], v[88:91]
	v_mfma_f32_16x16x32_bf16 v[104:107], v[152:155], v[176:179], v[104:107]
	v_mfma_f32_16x16x32_bf16 v[104:107], v[156:159], v[180:183], v[104:107]
	v_mfma_f32_16x16x32_bf16 v[122:125], v[152:155], v[168:171], v[122:125]
	v_mfma_f32_16x16x32_bf16 v[122:125], v[156:159], v[172:175], v[122:125]
	s_barrier
	s_mov_b32 m0, s35
	ds_read_b128 v[168:171], v221 offset:16384
	ds_read_b128 v[172:175], v221 offset:17408
	ds_read_b128 v[176:179], v221 offset:18432
	ds_read_b128 v[180:183], v221 offset:19456
	ds_read_b128 v[184:187], v221 offset:20480
	ds_read_b128 v[188:191], v221 offset:21504
	ds_read_b128 v[202:205], v221 offset:22528
	ds_read_b128 v[206:209], v221 offset:23552
	global_load_lds_dwordx4 v194, s[46:47]
	s_mov_b32 m0, s36
	s_nop 0
	s_add_u32 s70, s46, s90
	s_addc_u32 s71, s47, s91
	global_load_lds_dwordx4 v194, s[70:71]
	s_mov_b32 m0, s37
	s_nop 0
	s_add_u32 s70, s46, s48
	s_addc_u32 s71, s47, s49
	global_load_lds_dwordx4 v194, s[70:71]
	s_mov_b32 m0, s38
	s_nop 0
	s_add_u32 s70, s46, s52
	s_addc_u32 s71, s47, s53
	global_load_lds_dwordx4 v194, s[70:71]
	s_mov_b32 m0, s23
	s_nop 0
	global_load_lds_dwordx4 v196, s[44:45]
	s_mov_b32 m0, s24
	s_nop 0
	s_add_u32 s70, s44, s96
	s_addc_u32 s71, s45, s97
	global_load_lds_dwordx4 v196, s[70:71]
	s_waitcnt vmcnt(8)
	s_waitcnt lgkmcnt(0)
	s_barrier
	v_mfma_f32_16x16x32_bf16 v[64:67], v[136:139], v[168:171], v[64:67]
	v_mfma_f32_16x16x32_bf16 v[64:67], v[140:143], v[172:175], v[64:67]
	v_mfma_f32_16x16x32_bf16 v[48:51], v[136:139], v[176:179], v[48:51]
	v_mfma_f32_16x16x32_bf16 v[48:51], v[140:143], v[180:183], v[48:51]
	v_mfma_f32_16x16x32_bf16 v[32:35], v[136:139], v[184:187], v[32:35]
	v_mfma_f32_16x16x32_bf16 v[32:35], v[140:143], v[188:191], v[32:35]
	v_mfma_f32_16x16x32_bf16 v[16:19], v[136:139], v[202:205], v[16:19]
	v_mfma_f32_16x16x32_bf16 v[16:19], v[140:143], v[206:209], v[16:19]
	v_mfma_f32_16x16x32_bf16 v[12:15], v[144:147], v[202:205], v[12:15]
	v_mfma_f32_16x16x32_bf16 v[12:15], v[148:151], v[206:209], v[12:15]
	v_mfma_f32_16x16x32_bf16 v[28:31], v[144:147], v[184:187], v[28:31]
	v_mfma_f32_16x16x32_bf16 v[28:31], v[148:151], v[188:191], v[28:31]
	v_mfma_f32_16x16x32_bf16 v[44:47], v[144:147], v[176:179], v[44:47]
	v_mfma_f32_16x16x32_bf16 v[44:47], v[148:151], v[180:183], v[44:47]
	v_mfma_f32_16x16x32_bf16 v[60:63], v[144:147], v[168:171], v[60:63]
	v_mfma_f32_16x16x32_bf16 v[60:63], v[148:151], v[172:175], v[60:63]
	v_mfma_f32_16x16x32_bf16 v[52:55], v[160:163], v[168:171], v[52:55]
	v_mfma_f32_16x16x32_bf16 v[52:55], v[164:167], v[172:175], v[52:55]
	v_mfma_f32_16x16x32_bf16 v[36:39], v[160:163], v[176:179], v[36:39]
	v_mfma_f32_16x16x32_bf16 v[36:39], v[164:167], v[180:183], v[36:39]
	v_mfma_f32_16x16x32_bf16 v[20:23], v[160:163], v[184:187], v[20:23]
	v_mfma_f32_16x16x32_bf16 v[20:23], v[164:167], v[188:191], v[20:23]
	v_mfma_f32_16x16x32_bf16 v[4:7], v[160:163], v[202:205], v[4:7]
	v_mfma_f32_16x16x32_bf16 v[4:7], v[164:167], v[206:209], v[4:7]
	v_mfma_f32_16x16x32_bf16 v[8:11], v[152:155], v[202:205], v[8:11]
	v_mfma_f32_16x16x32_bf16 v[8:11], v[156:159], v[206:209], v[8:11]
	v_mfma_f32_16x16x32_bf16 v[24:27], v[152:155], v[184:187], v[24:27]
	v_mfma_f32_16x16x32_bf16 v[24:27], v[156:159], v[188:191], v[24:27]
	v_mfma_f32_16x16x32_bf16 v[40:43], v[152:155], v[176:179], v[40:43]
	v_mfma_f32_16x16x32_bf16 v[40:43], v[156:159], v[180:183], v[40:43]
	v_mfma_f32_16x16x32_bf16 v[56:59], v[152:155], v[168:171], v[56:59]
	v_mfma_f32_16x16x32_bf16 v[56:59], v[156:159], v[172:175], v[56:59]
	s_barrier
; #define PG8_MMA(ai, bj, At, Bt) do { __builtin_amdgcn_s_setprio(1); _Pragma("unroll") for (int m = 0; m < 4; ++m) _Pragma("unroll") for (int n = 0; n < 2; ++n) _Pragma("unroll") for (int k = 0; k < 2; ++k) \
;         acc[ai][bj][m][n] = __builtin_amdgcn_mfma_f32_16x16x32_bf16(Bt[n][k], At[m][k], acc[ai][bj][m][n], 0, 0, 0); __builtin_amdgcn_s_setprio(0); } while (0)
; #define PG8_WAIT_V(n) asm volatile("s_waitcnt vmcnt(" #n ")" ::: "memory")
; #define PG8_TRIP_HEAD(T) const int t = (T); const bool last = (t == nt - 2); \
;             const char* a1 = cA + (size_t)(t + 1) * kstep; \
;             const char* a2 = last ? nA : cA + (size_t)(t + 2) * kstep; const char* b2 = last ? nB : cB + (size_t)(t + 2) * kstep; \
;             const char* a3 = a2 + kstep; const char* b3 = b2 + kstep; \
;             if (last && has_next) S.a_ready(nxt);
; template <class Epi, class Sched, bool ALIGN_EPI = false, bool SP2 = false>
; __device__ __forceinline__ void gemm_phase(PG8_LAS unsigned char* lds, const Gemm g, const Sched& S, const Epi& E) {
;     ...
;         if constexpr (SP2) {
;             { PG8_TRIP_HEAD(0) PG8_TRIP_SP2(asm volatile("s_waitcnt vmcnt(%0)" :: "n"(8 + Epi::NST) : "memory"), PG8_MMAZ) }
;             for (int tt = 2; tt < nt; tt += 2) { PG8_TRIP_HEAD(tt) PG8_TRIP_SP2(PG8_WAIT_V(8), PG8_MMA) }
	ds_read_b128 v[136:139], v134
	ds_read_b128 v[140:143], v134 offset:1024
	ds_read_b128 v[144:147], v134 offset:2048
	ds_read_b128 v[148:151], v134 offset:3072
	ds_read_b128 v[152:155], v135
	ds_read_b128 v[156:159], v135 offset:1024
	ds_read_b128 v[160:163], v135 offset:2048
	ds_read_b128 v[164:167], v135 offset:3072
	s_mov_b32 m0, s25
	ds_read_b128 v[168:171], v221 offset:32768
	ds_read_b128 v[172:175], v221 offset:33792
	ds_read_b128 v[176:179], v221 offset:34816
	ds_read_b128 v[180:183], v221 offset:35840
	ds_read_b128 v[184:187], v221 offset:36864
	ds_read_b128 v[188:191], v221 offset:37888
	ds_read_b128 v[202:205], v221 offset:38912
	ds_read_b128 v[206:209], v221 offset:39936
	s_add_u32 s70, s44, s82
	s_addc_u32 s71, s45, s83
	global_load_lds_dwordx4 v196, s[70:71]
	s_mov_b32 m0, s26
	s_nop 0
	s_add_u32 s70, s44, s56
	s_addc_u32 s71, s45, s57
	global_load_lds_dwordx4 v196, s[70:71]
	s_waitcnt vmcnt(8)
	s_waitcnt lgkmcnt(0)
	s_barrier
	v_mfma_f32_16x16x32_bf16 v[130:133], v[136:139], v[168:171], v[130:133]
	v_mfma_f32_16x16x32_bf16 v[130:133], v[140:143], v[172:175], v[130:133]
	v_mfma_f32_16x16x32_bf16 v[112:115], v[136:139], v[176:179], v[112:115]
	v_mfma_f32_16x16x32_bf16 v[112:115], v[140:143], v[180:183], v[112:115]
	v_mfma_f32_16x16x32_bf16 v[96:99], v[136:139], v[184:187], v[96:99]
	v_mfma_f32_16x16x32_bf16 v[96:99], v[140:143], v[188:191], v[96:99]
	v_mfma_f32_16x16x32_bf16 v[80:83], v[136:139], v[202:205], v[80:83]
	v_mfma_f32_16x16x32_bf16 v[80:83], v[140:143], v[206:209], v[80:83]
	v_mfma_f32_16x16x32_bf16 v[76:79], v[144:147], v[202:205], v[76:79]
	v_mfma_f32_16x16x32_bf16 v[76:79], v[148:151], v[206:209], v[76:79]
	v_mfma_f32_16x16x32_bf16 v[92:95], v[144:147], v[184:187], v[92:95]
	v_mfma_f32_16x16x32_bf16 v[92:95], v[148:151], v[188:191], v[92:95]
	v_mfma_f32_16x16x32_bf16 v[108:111], v[144:147], v[176:179], v[108:111]
	v_mfma_f32_16x16x32_bf16 v[108:111], v[148:151], v[180:183], v[108:111]
	v_mfma_f32_16x16x32_bf16 v[126:129], v[144:147], v[168:171], v[126:129]
	v_mfma_f32_16x16x32_bf16 v[126:129], v[148:151], v[172:175], v[126:129]
	v_mfma_f32_16x16x32_bf16 v[118:121], v[160:163], v[168:171], v[118:121]
	v_mfma_f32_16x16x32_bf16 v[118:121], v[164:167], v[172:175], v[118:121]
	v_mfma_f32_16x16x32_bf16 v[100:103], v[160:163], v[176:179], v[100:103]
	v_mfma_f32_16x16x32_bf16 v[100:103], v[164:167], v[180:183], v[100:103]
	v_mfma_f32_16x16x32_bf16 v[84:87], v[160:163], v[184:187], v[84:87]
	v_mfma_f32_16x16x32_bf16 v[84:87], v[164:167], v[188:191], v[84:87]
	v_mfma_f32_16x16x32_bf16 v[68:71], v[160:163], v[202:205], v[68:71]
	v_mfma_f32_16x16x32_bf16 v[68:71], v[164:167], v[206:209], v[68:71]
	v_mfma_f32_16x16x32_bf16 v[72:75], v[152:155], v[202:205], v[72:75]
	v_mfma_f32_16x16x32_bf16 v[72:75], v[156:159], v[206:209], v[72:75]
	v_mfma_f32_16x16x32_bf16 v[88:91], v[152:155], v[184:187], v[88:91]
	v_mfma_f32_16x16x32_bf16 v[88:91], v[156:159], v[188:191], v[88:91]
	v_mfma_f32_16x16x32_bf16 v[104:107], v[152:155], v[176:179], v[104:107]
	v_mfma_f32_16x16x32_bf16 v[104:107], v[156:159], v[180:183], v[104:107]
	v_mfma_f32_16x16x32_bf16 v[122:125], v[152:155], v[168:171], v[122:125]
	v_mfma_f32_16x16x32_bf16 v[122:125], v[156:159], v[172:175], v[122:125]
	s_barrier
	s_mov_b32 m0, s39
	ds_read_b128 v[168:171], v221 offset:49152
	ds_read_b128 v[172:175], v221 offset:50176
	ds_read_b128 v[176:179], v221 offset:51200
	ds_read_b128 v[180:183], v221 offset:52224
	ds_read_b128 v[184:187], v221 offset:53248
	ds_read_b128 v[188:191], v221 offset:54272
	ds_read_b128 v[202:205], v221 offset:55296
	ds_read_b128 v[206:209], v221 offset:56320
	s_add_u32 s70, s46, s78
	s_addc_u32 s71, s47, s79
	global_load_lds_dwordx4 v194, s[70:71]
	s_mov_b32 m0, s40
	s_nop 0
	s_add_u32 s70, s46, s84
	s_addc_u32 s71, s47, s85
	global_load_lds_dwordx4 v194, s[70:71]
	s_mov_b32 m0, s41
	s_add_u32 s70, s46, s50
	s_addc_u32 s71, s47, s51
	global_load_lds_dwordx4 v194, s[70:71]
	s_mov_b32 m0, s42
	s_nop 0
	s_add_u32 s70, s46, s54
	s_addc_u32 s71, s47, s55
	global_load_lds_dwordx4 v194, s[70:71]
	s_mov_b32 m0, s27
	s_nop 0
	s_add_u32 s70, s44, s78
	s_addc_u32 s71, s45, s79
	global_load_lds_dwordx4 v196, s[70:71]
	s_mov_b32 m0, s28
	s_nop 0
	s_add_u32 s70, s44, s92
	s_addc_u32 s71, s45, s93
	global_load_lds_dwordx4 v196, s[70:71]
	s_waitcnt vmcnt(8)
	s_waitcnt lgkmcnt(0)
	s_barrier
	v_mfma_f32_16x16x32_bf16 v[64:67], v[136:139], v[168:171], v[64:67]
	v_mfma_f32_16x16x32_bf16 v[64:67], v[140:143], v[172:175], v[64:67]
	v_mfma_f32_16x16x32_bf16 v[48:51], v[136:139], v[176:179], v[48:51]
	v_mfma_f32_16x16x32_bf16 v[48:51], v[140:143], v[180:183], v[48:51]
	v_mfma_f32_16x16x32_bf16 v[32:35], v[136:139], v[184:187], v[32:35]
	v_mfma_f32_16x16x32_bf16 v[32:35], v[140:143], v[188:191], v[32:35]
	v_mfma_f32_16x16x32_bf16 v[16:19], v[136:139], v[202:205], v[16:19]
	v_mfma_f32_16x16x32_bf16 v[16:19], v[140:143], v[206:209], v[16:19]
	v_mfma_f32_16x16x32_bf16 v[12:15], v[144:147], v[202:205], v[12:15]
	v_mfma_f32_16x16x32_bf16 v[12:15], v[148:151], v[206:209], v[12:15]
	v_mfma_f32_16x16x32_bf16 v[28:31], v[144:147], v[184:187], v[28:31]
	v_mfma_f32_16x16x32_bf16 v[28:31], v[148:151], v[188:191], v[28:31]
	v_mfma_f32_16x16x32_bf16 v[44:47], v[144:147], v[176:179], v[44:47]
	v_mfma_f32_16x16x32_bf16 v[44:47], v[148:151], v[180:183], v[44:47]
	v_mfma_f32_16x16x32_bf16 v[60:63], v[144:147], v[168:171], v[60:63]
	v_mfma_f32_16x16x32_bf16 v[60:63], v[148:151], v[172:175], v[60:63]
	v_mfma_f32_16x16x32_bf16 v[52:55], v[160:163], v[168:171], v[52:55]
	v_mfma_f32_16x16x32_bf16 v[52:55], v[164:167], v[172:175], v[52:55]
	v_mfma_f32_16x16x32_bf16 v[36:39], v[160:163], v[176:179], v[36:39]
	v_mfma_f32_16x16x32_bf16 v[36:39], v[164:167], v[180:183], v[36:39]
	v_mfma_f32_16x16x32_bf16 v[20:23], v[160:163], v[184:187], v[20:23]
	v_mfma_f32_16x16x32_bf16 v[20:23], v[164:167], v[188:191], v[20:23]
	v_mfma_f32_16x16x32_bf16 v[4:7], v[160:163], v[202:205], v[4:7]
	v_mfma_f32_16x16x32_bf16 v[4:7], v[164:167], v[206:209], v[4:7]
	v_mfma_f32_16x16x32_bf16 v[8:11], v[152:155], v[202:205], v[8:11]
	v_mfma_f32_16x16x32_bf16 v[8:11], v[156:159], v[206:209], v[8:11]
	v_mfma_f32_16x16x32_bf16 v[24:27], v[152:155], v[184:187], v[24:27]
	v_mfma_f32_16x16x32_bf16 v[24:27], v[156:159], v[188:191], v[24:27]
	v_mfma_f32_16x16x32_bf16 v[40:43], v[152:155], v[176:179], v[40:43]
	v_mfma_f32_16x16x32_bf16 v[40:43], v[156:159], v[180:183], v[40:43]
	v_mfma_f32_16x16x32_bf16 v[56:59], v[152:155], v[168:171], v[56:59]
	v_mfma_f32_16x16x32_bf16 v[56:59], v[156:159], v[172:175], v[56:59]
	s_barrier
	s_add_i32 s15, s15, 2
	s_add_u32 s20, s20, 0x100
	s_addc_u32 s21, s21, 0
	s_add_u32 s8, s8, 0x100
	s_addc_u32 s9, s9, 0
	s_cmp_gt_u32 s15, 29
	s_cbranch_scc0 .LBB0_594
	s_and_b64 vcc, exec, s[12:13]
	s_cbranch_vccz .LBB0_597
	s_barrier

.LBB0_700:
	ds_read_b128 v[120:123], v116
	ds_read_b128 v[132:135], v116 offset:1024
	ds_read_b128 v[144:147], v116 offset:2048
	ds_read_b128 v[148:151], v116 offset:3072
	ds_read_b128 v[152:155], v117
	ds_read_b128 v[156:159], v117 offset:1024
	ds_read_b128 v[166:169], v117 offset:2048
	ds_read_b128 v[170:173], v117 offset:3072
	s_add_u32 s27, s10, 0xfff7c080
	s_addc_u32 s47, s11, -1
	s_cmp_eq_u32 s26, 28
	s_cselect_b32 s49, s21, s47
	s_cselect_b32 s48, s20, s27
	s_cselect_b32 s51, s3, s25
	s_cselect_b32 s50, s4, s24
	s_mov_b32 m0, s5
	ds_read_b128 v[180:183], v178
	ds_read_b128 v[184:187], v178 offset:1024
	ds_read_b128 v[188:191], v178 offset:2048
	ds_read_b128 v[192:195], v178 offset:3072
	ds_read_b128 v[196:199], v178 offset:4096
	ds_read_b128 v[200:203], v178 offset:5120
	ds_read_b128 v[204:207], v178 offset:6144
	ds_read_b128 v[214:217], v178 offset:7168
	global_load_lds_dwordx4 v164, s[10:11]
	s_mov_b32 m0, s19
	s_nop 0
	s_add_u32 s70, s10, s96
	s_addc_u32 s71, s11, s97
	global_load_lds_dwordx4 v164, s[70:71]
	s_waitcnt vmcnt(8)
	s_waitcnt lgkmcnt(0)
	s_barrier
	v_mfma_f32_16x16x32_bf16 v[140:143], v[120:123], v[180:183], v[140:143]
	v_mfma_f32_16x16x32_bf16 v[140:143], v[132:135], v[184:187], v[140:143]
	v_mfma_f32_16x16x32_bf16 v[112:115], v[120:123], v[188:191], v[112:115]
	v_mfma_f32_16x16x32_bf16 v[112:115], v[132:135], v[192:195], v[112:115]
	v_mfma_f32_16x16x32_bf16 v[96:99], v[120:123], v[196:199], v[96:99]
	v_mfma_f32_16x16x32_bf16 v[96:99], v[132:135], v[200:203], v[96:99]
	v_mfma_f32_16x16x32_bf16 v[80:83], v[120:123], v[204:207], v[80:83]
	v_mfma_f32_16x16x32_bf16 v[80:83], v[132:135], v[214:217], v[80:83]
	v_mfma_f32_16x16x32_bf16 v[76:79], v[144:147], v[204:207], v[76:79]
	v_mfma_f32_16x16x32_bf16 v[76:79], v[148:151], v[214:217], v[76:79]
	v_mfma_f32_16x16x32_bf16 v[92:95], v[144:147], v[196:199], v[92:95]
	v_mfma_f32_16x16x32_bf16 v[92:95], v[148:151], v[200:203], v[92:95]
	v_mfma_f32_16x16x32_bf16 v[108:111], v[144:147], v[188:191], v[108:111]
	v_mfma_f32_16x16x32_bf16 v[108:111], v[148:151], v[192:195], v[108:111]
	v_mfma_f32_16x16x32_bf16 v[136:139], v[144:147], v[180:183], v[136:139]
	v_mfma_f32_16x16x32_bf16 v[136:139], v[148:151], v[184:187], v[136:139]
	v_mfma_f32_16x16x32_bf16 v[124:127], v[166:169], v[180:183], v[124:127]
	v_mfma_f32_16x16x32_bf16 v[124:127], v[170:173], v[184:187], v[124:127]
	v_mfma_f32_16x16x32_bf16 v[100:103], v[166:169], v[188:191], v[100:103]
	v_mfma_f32_16x16x32_bf16 v[100:103], v[170:173], v[192:195], v[100:103]
	v_mfma_f32_16x16x32_bf16 v[84:87], v[166:169], v[196:199], v[84:87]
	v_mfma_f32_16x16x32_bf16 v[84:87], v[170:173], v[200:203], v[84:87]
	v_mfma_f32_16x16x32_bf16 v[68:71], v[166:169], v[204:207], v[68:71]
	v_mfma_f32_16x16x32_bf16 v[68:71], v[170:173], v[214:217], v[68:71]
	v_mfma_f32_16x16x32_bf16 v[72:75], v[152:155], v[204:207], v[72:75]
	v_mfma_f32_16x16x32_bf16 v[72:75], v[156:159], v[214:217], v[72:75]
	v_mfma_f32_16x16x32_bf16 v[88:91], v[152:155], v[196:199], v[88:91]
	v_mfma_f32_16x16x32_bf16 v[88:91], v[156:159], v[200:203], v[88:91]
	v_mfma_f32_16x16x32_bf16 v[104:107], v[152:155], v[188:191], v[104:107]
	v_mfma_f32_16x16x32_bf16 v[104:107], v[156:159], v[192:195], v[104:107]
	v_mfma_f32_16x16x32_bf16 v[128:131], v[152:155], v[180:183], v[128:131]
	v_mfma_f32_16x16x32_bf16 v[128:131], v[156:159], v[184:187], v[128:131]
	s_barrier
	s_mov_b32 m0, s33
	ds_read_b128 v[180:183], v178 offset:16384
	ds_read_b128 v[184:187], v178 offset:17408
	ds_read_b128 v[188:191], v178 offset:18432
	ds_read_b128 v[192:195], v178 offset:19456
	ds_read_b128 v[196:199], v178 offset:20480
	ds_read_b128 v[200:203], v178 offset:21504
	ds_read_b128 v[204:207], v178 offset:22528
	ds_read_b128 v[214:217], v178 offset:23552
	global_load_lds_dwordx4 v160, s[50:51]
	s_mov_b32 m0, s40
	s_nop 0
	s_add_u32 s70, s50, s90
	s_addc_u32 s71, s51, s91
	global_load_lds_dwordx4 v160, s[70:71]
	s_mov_b32 m0, s41
	s_nop 0
	s_add_u32 s70, s50, s52
	s_addc_u32 s71, s51, s53
	global_load_lds_dwordx4 v160, s[70:71]
	s_mov_b32 m0, s42
	s_nop 0
	s_add_u32 s70, s50, s56
	s_addc_u32 s71, s51, s57
	global_load_lds_dwordx4 v160, s[70:71]
	s_mov_b32 m0, s29
	s_nop 0
	global_load_lds_dwordx4 v162, s[48:49]
	s_mov_b32 m0, s30
	s_nop 0
	s_add_u32 s70, s48, s96
	s_addc_u32 s71, s49, s97
	global_load_lds_dwordx4 v162, s[70:71]
	s_waitcnt vmcnt(8)
	s_waitcnt lgkmcnt(0)
	s_barrier
	v_mfma_f32_16x16x32_bf16 v[56:59], v[120:123], v[180:183], v[56:59]
	v_mfma_f32_16x16x32_bf16 v[56:59], v[132:135], v[184:187], v[56:59]
	v_mfma_f32_16x16x32_bf16 v[48:51], v[120:123], v[188:191], v[48:51]
	v_mfma_f32_16x16x32_bf16 v[48:51], v[132:135], v[192:195], v[48:51]
	v_mfma_f32_16x16x32_bf16 v[32:35], v[120:123], v[196:199], v[32:35]
	v_mfma_f32_16x16x32_bf16 v[32:35], v[132:135], v[200:203], v[32:35]
	v_mfma_f32_16x16x32_bf16 v[16:19], v[120:123], v[204:207], v[16:19]
	v_mfma_f32_16x16x32_bf16 v[16:19], v[132:135], v[214:217], v[16:19]
	v_mfma_f32_16x16x32_bf16 v[12:15], v[144:147], v[204:207], v[12:15]
	v_mfma_f32_16x16x32_bf16 v[12:15], v[148:151], v[214:217], v[12:15]
	v_mfma_f32_16x16x32_bf16 v[28:31], v[144:147], v[196:199], v[28:31]
	v_mfma_f32_16x16x32_bf16 v[28:31], v[148:151], v[200:203], v[28:31]
	v_mfma_f32_16x16x32_bf16 v[44:47], v[144:147], v[188:191], v[44:47]
	v_mfma_f32_16x16x32_bf16 v[44:47], v[148:151], v[192:195], v[44:47]
	v_mfma_f32_16x16x32_bf16 v[52:55], v[144:147], v[180:183], v[52:55]
	v_mfma_f32_16x16x32_bf16 v[52:55], v[148:151], v[184:187], v[52:55]
	v_mfma_f32_16x16x32_bf16 v[60:63], v[166:169], v[180:183], v[60:63]
	v_mfma_f32_16x16x32_bf16 v[60:63], v[170:173], v[184:187], v[60:63]
	v_mfma_f32_16x16x32_bf16 v[36:39], v[166:169], v[188:191], v[36:39]
	v_mfma_f32_16x16x32_bf16 v[36:39], v[170:173], v[192:195], v[36:39]
	v_mfma_f32_16x16x32_bf16 v[20:23], v[166:169], v[196:199], v[20:23]
	v_mfma_f32_16x16x32_bf16 v[20:23], v[170:173], v[200:203], v[20:23]
	v_mfma_f32_16x16x32_bf16 v[4:7], v[166:169], v[204:207], v[4:7]
	v_mfma_f32_16x16x32_bf16 v[4:7], v[170:173], v[214:217], v[4:7]
	v_mfma_f32_16x16x32_bf16 v[8:11], v[152:155], v[204:207], v[8:11]
	v_mfma_f32_16x16x32_bf16 v[8:11], v[156:159], v[214:217], v[8:11]
	v_mfma_f32_16x16x32_bf16 v[24:27], v[152:155], v[196:199], v[24:27]
	v_mfma_f32_16x16x32_bf16 v[24:27], v[156:159], v[200:203], v[24:27]
	v_mfma_f32_16x16x32_bf16 v[40:43], v[152:155], v[188:191], v[40:43]
	v_mfma_f32_16x16x32_bf16 v[40:43], v[156:159], v[192:195], v[40:43]
	v_mfma_f32_16x16x32_bf16 v[64:67], v[152:155], v[180:183], v[64:67]
	v_mfma_f32_16x16x32_bf16 v[64:67], v[156:159], v[184:187], v[64:67]
	s_barrier
; #define PG8_MMA(ai, bj, At, Bt) do { __builtin_amdgcn_s_setprio(1); _Pragma("unroll") for (int m = 0; m < 4; ++m) _Pragma("unroll") for (int n = 0; n < 2; ++n) _Pragma("unroll") for (int k = 0; k < 2; ++k) \
;         acc[ai][bj][m][n] = __builtin_amdgcn_mfma_f32_16x16x32_bf16(Bt[n][k], At[m][k], acc[ai][bj][m][n], 0, 0, 0); __builtin_amdgcn_s_setprio(0); } while (0)
; #define PG8_WAIT_V(n) asm volatile("s_waitcnt vmcnt(" #n ")" ::: "memory")
; #define PG8_TRIP_HEAD(T) const int t = (T); const bool last = (t == nt - 2); \
;             const char* a1 = cA + (size_t)(t + 1) * kstep; \
;             const char* a2 = last ? nA : cA + (size_t)(t + 2) * kstep; const char* b2 = last ? nB : cB + (size_t)(t + 2) * kstep; \
;             const char* a3 = a2 + kstep; const char* b3 = b2 + kstep; \
;             if (last && has_next) S.a_ready(nxt);
; template <class Epi, class Sched, bool ALIGN_EPI = false, bool SP2 = false>
; __device__ __forceinline__ void gemm_phase(PG8_LAS unsigned char* lds, const Gemm g, const Sched& S, const Epi& E) {
;     ...
;         if constexpr (SP2) {
;             { PG8_TRIP_HEAD(0) PG8_TRIP_SP2(asm volatile("s_waitcnt vmcnt(%0)" :: "n"(8 + Epi::NST) : "memory"), PG8_MMAZ) }
;             for (int tt = 2; tt < nt; tt += 2) { PG8_TRIP_HEAD(tt) PG8_TRIP_SP2(PG8_WAIT_V(8), PG8_MMA) }
	ds_read_b128 v[120:123], v118
	ds_read_b128 v[132:135], v118 offset:1024
	ds_read_b128 v[144:147], v118 offset:2048
	ds_read_b128 v[148:151], v118 offset:3072
	ds_read_b128 v[152:155], v119
	ds_read_b128 v[156:159], v119 offset:1024
	ds_read_b128 v[166:169], v119 offset:2048
	ds_read_b128 v[170:173], v119 offset:3072
	s_mov_b32 m0, s31
	ds_read_b128 v[180:183], v178 offset:32768
	ds_read_b128 v[184:187], v178 offset:33792
	ds_read_b128 v[188:191], v178 offset:34816
	ds_read_b128 v[192:195], v178 offset:35840
	ds_read_b128 v[196:199], v178 offset:36864
	ds_read_b128 v[200:203], v178 offset:37888
	ds_read_b128 v[204:207], v178 offset:38912
	ds_read_b128 v[214:217], v178 offset:39936
	s_add_u32 s70, s48, s82
	s_addc_u32 s71, s49, s83
	global_load_lds_dwordx4 v162, s[70:71]
	s_mov_b32 m0, s34
	s_nop 0
	s_add_u32 s70, s48, s62
	s_addc_u32 s71, s49, s63
	global_load_lds_dwordx4 v162, s[70:71]
	s_waitcnt vmcnt(8)
	s_waitcnt lgkmcnt(0)
	s_barrier
	v_mfma_f32_16x16x32_bf16 v[140:143], v[120:123], v[180:183], v[140:143]
	v_mfma_f32_16x16x32_bf16 v[140:143], v[132:135], v[184:187], v[140:143]
	v_mfma_f32_16x16x32_bf16 v[112:115], v[120:123], v[188:191], v[112:115]
	v_mfma_f32_16x16x32_bf16 v[112:115], v[132:135], v[192:195], v[112:115]
	v_mfma_f32_16x16x32_bf16 v[96:99], v[120:123], v[196:199], v[96:99]
	v_mfma_f32_16x16x32_bf16 v[96:99], v[132:135], v[200:203], v[96:99]
	v_mfma_f32_16x16x32_bf16 v[80:83], v[120:123], v[204:207], v[80:83]
	v_mfma_f32_16x16x32_bf16 v[80:83], v[132:135], v[214:217], v[80:83]
	v_mfma_f32_16x16x32_bf16 v[76:79], v[144:147], v[204:207], v[76:79]
	v_mfma_f32_16x16x32_bf16 v[76:79], v[148:151], v[214:217], v[76:79]
	v_mfma_f32_16x16x32_bf16 v[92:95], v[144:147], v[196:199], v[92:95]
	v_mfma_f32_16x16x32_bf16 v[92:95], v[148:151], v[200:203], v[92:95]
	v_mfma_f32_16x16x32_bf16 v[108:111], v[144:147], v[188:191], v[108:111]
	v_mfma_f32_16x16x32_bf16 v[108:111], v[148:151], v[192:195], v[108:111]
	v_mfma_f32_16x16x32_bf16 v[136:139], v[144:147], v[180:183], v[136:139]
	v_mfma_f32_16x16x32_bf16 v[136:139], v[148:151], v[184:187], v[136:139]
	v_mfma_f32_16x16x32_bf16 v[124:127], v[166:169], v[180:183], v[124:127]
	v_mfma_f32_16x16x32_bf16 v[124:127], v[170:173], v[184:187], v[124:127]
	v_mfma_f32_16x16x32_bf16 v[100:103], v[166:169], v[188:191], v[100:103]
	v_mfma_f32_16x16x32_bf16 v[100:103], v[170:173], v[192:195], v[100:103]
	v_mfma_f32_16x16x32_bf16 v[84:87], v[166:169], v[196:199], v[84:87]
	v_mfma_f32_16x16x32_bf16 v[84:87], v[170:173], v[200:203], v[84:87]
	v_mfma_f32_16x16x32_bf16 v[68:71], v[166:169], v[204:207], v[68:71]
	v_mfma_f32_16x16x32_bf16 v[68:71], v[170:173], v[214:217], v[68:71]
	v_mfma_f32_16x16x32_bf16 v[72:75], v[152:155], v[204:207], v[72:75]
	v_mfma_f32_16x16x32_bf16 v[72:75], v[156:159], v[214:217], v[72:75]
	v_mfma_f32_16x16x32_bf16 v[88:91], v[152:155], v[196:199], v[88:91]
	v_mfma_f32_16x16x32_bf16 v[88:91], v[156:159], v[200:203], v[88:91]
	v_mfma_f32_16x16x32_bf16 v[104:107], v[152:155], v[188:191], v[104:107]
	v_mfma_f32_16x16x32_bf16 v[104:107], v[156:159], v[192:195], v[104:107]
	v_mfma_f32_16x16x32_bf16 v[128:131], v[152:155], v[180:183], v[128:131]
	v_mfma_f32_16x16x32_bf16 v[128:131], v[156:159], v[184:187], v[128:131]
	s_barrier
	s_mov_b32 m0, s43
	ds_read_b128 v[180:183], v178 offset:49152
	ds_read_b128 v[184:187], v178 offset:50176
	ds_read_b128 v[188:191], v178 offset:51200
	ds_read_b128 v[192:195], v178 offset:52224
	ds_read_b128 v[196:199], v178 offset:53248
	ds_read_b128 v[200:203], v178 offset:54272
	ds_read_b128 v[204:207], v178 offset:55296
	ds_read_b128 v[214:217], v178 offset:56320
	s_add_u32 s70, s50, s78
	s_addc_u32 s71, s51, s79
	global_load_lds_dwordx4 v160, s[70:71]
	s_mov_b32 m0, s44
	s_nop 0
	s_add_u32 s70, s50, s84
	s_addc_u32 s71, s51, s85
	global_load_lds_dwordx4 v160, s[70:71]
	s_mov_b32 m0, s45
	s_add_u32 s70, s50, s54
	s_addc_u32 s71, s51, s55
	global_load_lds_dwordx4 v160, s[70:71]
	s_mov_b32 m0, s46
	s_nop 0
	s_add_u32 s70, s50, s60
	s_addc_u32 s71, s51, s61
	global_load_lds_dwordx4 v160, s[70:71]
	s_mov_b32 m0, s36
	s_nop 0
	s_add_u32 s70, s48, s78
	s_addc_u32 s71, s49, s79
	global_load_lds_dwordx4 v162, s[70:71]
	s_mov_b32 m0, s37
	s_nop 0
	s_add_u32 s70, s48, s92
	s_addc_u32 s71, s49, s93
	global_load_lds_dwordx4 v162, s[70:71]
	s_waitcnt vmcnt(8)
	s_waitcnt lgkmcnt(0)
	s_barrier
	v_mfma_f32_16x16x32_bf16 v[56:59], v[120:123], v[180:183], v[56:59]
	v_mfma_f32_16x16x32_bf16 v[56:59], v[132:135], v[184:187], v[56:59]
	v_mfma_f32_16x16x32_bf16 v[48:51], v[120:123], v[188:191], v[48:51]
	v_mfma_f32_16x16x32_bf16 v[48:51], v[132:135], v[192:195], v[48:51]
	v_mfma_f32_16x16x32_bf16 v[32:35], v[120:123], v[196:199], v[32:35]
	v_mfma_f32_16x16x32_bf16 v[32:35], v[132:135], v[200:203], v[32:35]
	v_mfma_f32_16x16x32_bf16 v[16:19], v[120:123], v[204:207], v[16:19]
	v_mfma_f32_16x16x32_bf16 v[16:19], v[132:135], v[214:217], v[16:19]
	v_mfma_f32_16x16x32_bf16 v[12:15], v[144:147], v[204:207], v[12:15]
	v_mfma_f32_16x16x32_bf16 v[12:15], v[148:151], v[214:217], v[12:15]
	v_mfma_f32_16x16x32_bf16 v[28:31], v[144:147], v[196:199], v[28:31]
	v_mfma_f32_16x16x32_bf16 v[28:31], v[148:151], v[200:203], v[28:31]
	v_mfma_f32_16x16x32_bf16 v[44:47], v[144:147], v[188:191], v[44:47]
	v_mfma_f32_16x16x32_bf16 v[44:47], v[148:151], v[192:195], v[44:47]
	v_mfma_f32_16x16x32_bf16 v[52:55], v[144:147], v[180:183], v[52:55]
	v_mfma_f32_16x16x32_bf16 v[52:55], v[148:151], v[184:187], v[52:55]
	v_mfma_f32_16x16x32_bf16 v[60:63], v[166:169], v[180:183], v[60:63]
	v_mfma_f32_16x16x32_bf16 v[60:63], v[170:173], v[184:187], v[60:63]
	v_mfma_f32_16x16x32_bf16 v[36:39], v[166:169], v[188:191], v[36:39]
	v_mfma_f32_16x16x32_bf16 v[36:39], v[170:173], v[192:195], v[36:39]
	v_mfma_f32_16x16x32_bf16 v[20:23], v[166:169], v[196:199], v[20:23]
	v_mfma_f32_16x16x32_bf16 v[20:23], v[170:173], v[200:203], v[20:23]
	v_mfma_f32_16x16x32_bf16 v[4:7], v[166:169], v[204:207], v[4:7]
	v_mfma_f32_16x16x32_bf16 v[4:7], v[170:173], v[214:217], v[4:7]
	v_mfma_f32_16x16x32_bf16 v[8:11], v[152:155], v[204:207], v[8:11]
	v_mfma_f32_16x16x32_bf16 v[8:11], v[156:159], v[214:217], v[8:11]
	v_mfma_f32_16x16x32_bf16 v[24:27], v[152:155], v[196:199], v[24:27]
	v_mfma_f32_16x16x32_bf16 v[24:27], v[156:159], v[200:203], v[24:27]
	v_mfma_f32_16x16x32_bf16 v[40:43], v[152:155], v[188:191], v[40:43]
	v_mfma_f32_16x16x32_bf16 v[40:43], v[156:159], v[192:195], v[40:43]
	v_mfma_f32_16x16x32_bf16 v[64:67], v[152:155], v[180:183], v[64:67]
	v_mfma_f32_16x16x32_bf16 v[64:67], v[156:159], v[184:187], v[64:67]
	s_barrier
	s_add_i32 s26, s26, 2
	s_add_u32 s10, s10, 0x100
	s_addc_u32 s11, s11, 0
	s_add_u32 s24, s24, 0x100
	s_addc_u32 s25, s25, 0
	s_cmp_gt_u32 s26, 29
	s_cbranch_scc0 .LBB0_700
	s_and_b64 vcc, exec, s[16:17]
	s_cbranch_vccz .LBB0_703
	s_barrier
